# SGU epilogue: u-values of a 16-token block fetched together instead of one load-wait per step; NSA selected-branch unit descriptor carried across iterations
# speedup vs baseline: 1.0112x; 1.0038x over previous
.LBB0_381:
	v_readlane_b32 s14, v252, 48
	v_readlane_b32 s15, v252, 49
	v_or_b32_e32 v46, s25, v186
	s_movk_i32 s16, 0x2800
	v_mov_b64_e32 v[56:57], s[14:15]
	v_mad_i64_i32 v[34:35], s[10:11], v46, s16, v[56:57]
	s_mov_b64 s[18:19], 0x1600
	v_lshl_add_u64 v[40:41], v[34:35], 0, s[18:19]
	v_lshlrev_b64 v[54:55], 1, v[90:91]
	v_lshl_add_u64 v[44:45], v[40:41], 0, v[54:55]
	s_waitcnt lgkmcnt(0)
	s_barrier
	global_load_dwordx4 v[30:33], v[104:105], off
	global_load_dword v42, v[106:107], off
	v_ashrrev_i32_e32 v47, 31, v46
	global_load_dwordx2 v[44:45], v[44:45], off
	v_lshlrev_b64 v[38:39], 10, v[46:47]
	ds_read_b128 v[34:37], v193
	v_lshlrev_b64 v[52:53], 1, v[92:93]
	v_lshl_add_u64 v[38:39], v[138:139], 0, v[38:39]
	v_lshlrev_b64 v[48:49], 1, v[94:95]
	v_lshlrev_b64 v[50:51], 1, v[96:97]
	v_lshl_add_u64 v[216:217], v[40:41], 0, v[52:53]
	global_load_dwordx2 v[216:217], v[216:217], off
	v_lshl_add_u64 v[218:219], v[40:41], 0, v[48:49]
	global_load_dwordx2 v[218:219], v[218:219], off
	v_lshl_add_u64 v[220:221], v[40:41], 0, v[50:51]
	global_load_dwordx2 v[220:221], v[220:221], off
	s_mov_b32 s9, 6
	s_waitcnt vmcnt(2) lgkmcnt(0)
	v_mfma_f32_16x16x32_bf16 v[34:37], v[34:37], v[30:33], 0
	s_waitcnt vmcnt(0)
	v_lshlrev_b32_e32 v43, 16, v44
	v_mul_f32_e32 v47, 0x3d372713, v43
	v_mul_f32_e32 v47, v47, v43
	v_fma_f32 v47, v47, v43, v43
	v_mul_f32_e32 v47, 0xc0135761, v47
	v_exp_f32_e32 v47, v47
	s_nop 0
	v_add_f32_e32 v34, v42, v34
	v_add_f32_e32 v35, v42, v35
	v_add_f32_e32 v36, v42, v36
	v_add_f32_e32 v47, 1.0, v47
	v_rcp_f32_e32 v47, v47
	v_add_f32_e32 v37, v42, v37
	v_mul_f32_e32 v43, v47, v43
	v_mul_f32_e32 v34, v34, v43
	v_and_b32_e32 v43, 0xffff0000, v44
	v_mul_f32_e32 v44, 0x3d372713, v43
	v_mul_f32_e32 v44, v44, v43
	v_fma_f32 v44, v44, v43, v43
	v_mul_f32_e32 v44, 0xc0135761, v44
	v_exp_f32_e32 v44, v44
	s_nop 0
	v_add_f32_e32 v44, 1.0, v44
	v_rcp_f32_e32 v44, v44
	s_nop 0
	v_mul_f32_e32 v43, v44, v43
	v_mul_f32_e32 v35, v35, v43
	v_cvt_pk_bf16_f32 v34, v34, v35
	v_lshlrev_b32_e32 v35, 16, v45
	v_mul_f32_e32 v43, 0x3d372713, v35
	v_mul_f32_e32 v43, v43, v35
	v_fma_f32 v43, v43, v35, v35
	v_mul_f32_e32 v43, 0xc0135761, v43
	v_exp_f32_e32 v43, v43
	s_nop 0
	v_add_f32_e32 v43, 1.0, v43
	v_rcp_f32_e32 v43, v43
	s_nop 0
	v_mul_f32_e32 v35, v43, v35
	v_mul_f32_e32 v35, v36, v35
	v_and_b32_e32 v36, 0xffff0000, v45
	v_mul_f32_e32 v43, 0x3d372713, v36
	v_mul_f32_e32 v43, v43, v36
	v_fma_f32 v43, v43, v36, v36
	v_mul_f32_e32 v43, 0xc0135761, v43
	v_exp_f32_e32 v43, v43
	v_lshl_add_u64 v[44:45], v[40:41], 0, v[52:53]
	v_add_f32_e32 v43, 1.0, v43
	v_rcp_f32_e32 v43, v43
	s_nop 0
	v_mul_f32_e32 v36, v43, v36
	v_mul_f32_e32 v36, v37, v36
	v_cvt_pk_bf16_f32 v35, v35, v36
	s_waitcnt vmcnt(2)
	v_mov_b64_e32 v[44:45], v[216:217]
	v_lshlrev_b32_e32 v43, 16, v44
	global_store_dwordx2 v[38:39], v[34:35], off
	ds_read_b128 v[34:37], v193 offset:4352
	v_mul_f32_e32 v47, 0x3d372713, v43
	v_mul_f32_e32 v47, v47, v43
	v_fma_f32 v47, v47, v43, v43
	v_mul_f32_e32 v47, 0xc0135761, v47
	v_exp_f32_e32 v47, v47
	s_waitcnt lgkmcnt(0)
	v_mfma_f32_16x16x32_bf16 v[34:37], v[34:37], v[30:33], 0
	v_add_f32_e32 v47, 1.0, v47
	v_rcp_f32_e32 v47, v47
	s_nop 5
	v_add_f32_e32 v34, v42, v34
	v_add_f32_e32 v35, v42, v35
	v_mul_f32_e32 v43, v47, v43
	v_mul_f32_e32 v34, v34, v43
	v_and_b32_e32 v43, 0xffff0000, v44
	v_mul_f32_e32 v44, 0x3d372713, v43
	v_mul_f32_e32 v44, v44, v43
	v_fma_f32 v44, v44, v43, v43
	v_mul_f32_e32 v44, 0xc0135761, v44
	v_exp_f32_e32 v44, v44
	v_add_f32_e32 v36, v42, v36
	v_add_f32_e32 v37, v42, v37
	v_add_f32_e32 v44, 1.0, v44
	v_rcp_f32_e32 v44, v44
	s_nop 0
	v_mul_f32_e32 v43, v44, v43
	v_mul_f32_e32 v35, v35, v43
	v_cvt_pk_bf16_f32 v34, v34, v35
	v_lshlrev_b32_e32 v35, 16, v45
	v_mul_f32_e32 v43, 0x3d372713, v35
	v_mul_f32_e32 v43, v43, v35
	v_fma_f32 v43, v43, v35, v35
	v_mul_f32_e32 v43, 0xc0135761, v43
	v_exp_f32_e32 v43, v43
	s_nop 0
	v_add_f32_e32 v43, 1.0, v43
	v_rcp_f32_e32 v43, v43
	s_nop 0
	v_mul_f32_e32 v35, v43, v35
	v_mul_f32_e32 v35, v36, v35
	v_and_b32_e32 v36, 0xffff0000, v45
	v_mul_f32_e32 v43, 0x3d372713, v36
	v_mul_f32_e32 v43, v43, v36
	v_fma_f32 v43, v43, v36, v36
	v_mul_f32_e32 v43, 0xc0135761, v43
	v_exp_f32_e32 v43, v43
	v_lshl_add_u64 v[44:45], v[40:41], 0, v[48:49]
	v_add_f32_e32 v43, 1.0, v43
	v_rcp_f32_e32 v43, v43
	s_nop 0
	v_mul_f32_e32 v36, v43, v36
	v_mul_f32_e32 v36, v37, v36
	v_cvt_pk_bf16_f32 v35, v35, v36
	s_waitcnt vmcnt(2)
	v_mov_b64_e32 v[44:45], v[218:219]
	v_lshlrev_b32_e32 v43, 16, v44
	global_store_dwordx2 v[38:39], v[34:35], off offset:32
	ds_read_b128 v[34:37], v193 offset:8704
	v_mul_f32_e32 v47, 0x3d372713, v43
	v_mul_f32_e32 v47, v47, v43
	v_fma_f32 v47, v47, v43, v43
	v_mul_f32_e32 v47, 0xc0135761, v47
	v_exp_f32_e32 v47, v47
	s_waitcnt lgkmcnt(0)
	v_mfma_f32_16x16x32_bf16 v[34:37], v[34:37], v[30:33], 0
	v_add_f32_e32 v47, 1.0, v47
	v_rcp_f32_e32 v47, v47
	s_nop 5
	v_add_f32_e32 v34, v42, v34
	v_add_f32_e32 v35, v42, v35
	v_mul_f32_e32 v43, v47, v43
	v_mul_f32_e32 v34, v34, v43
	v_and_b32_e32 v43, 0xffff0000, v44
	v_mul_f32_e32 v44, 0x3d372713, v43
	v_mul_f32_e32 v44, v44, v43
	v_fma_f32 v44, v44, v43, v43
	v_mul_f32_e32 v44, 0xc0135761, v44
	v_exp_f32_e32 v44, v44
	v_add_f32_e32 v36, v42, v36
	v_add_f32_e32 v37, v42, v37
	v_add_f32_e32 v44, 1.0, v44
	v_rcp_f32_e32 v44, v44
	s_nop 0
	v_mul_f32_e32 v43, v44, v43
	v_mul_f32_e32 v35, v35, v43
	v_cvt_pk_bf16_f32 v34, v34, v35
	v_lshlrev_b32_e32 v35, 16, v45
	v_mul_f32_e32 v43, 0x3d372713, v35
	v_mul_f32_e32 v43, v43, v35
	v_fma_f32 v43, v43, v35, v35
	v_mul_f32_e32 v43, 0xc0135761, v43
	v_exp_f32_e32 v43, v43
	s_nop 0
	v_add_f32_e32 v43, 1.0, v43
	v_rcp_f32_e32 v43, v43
	s_nop 0
	v_mul_f32_e32 v35, v43, v35
	v_mul_f32_e32 v35, v36, v35
	v_and_b32_e32 v36, 0xffff0000, v45
	v_mul_f32_e32 v43, 0x3d372713, v36
	v_mul_f32_e32 v43, v43, v36
	v_fma_f32 v43, v43, v36, v36
	v_mul_f32_e32 v43, 0xc0135761, v43
	v_exp_f32_e32 v43, v43
	s_nop 0
	v_add_f32_e32 v43, 1.0, v43
	v_rcp_f32_e32 v43, v43
	s_nop 0
	v_mul_f32_e32 v36, v43, v36
	v_mul_f32_e32 v36, v37, v36
	v_cvt_pk_bf16_f32 v35, v35, v36
	global_store_dwordx2 v[38:39], v[34:35], off offset:64
	ds_read_b128 v[34:37], v193 offset:13056
	s_waitcnt lgkmcnt(0)
	v_mfma_f32_16x16x32_bf16 v[30:33], v[34:37], v[30:33], 0
	v_lshl_add_u64 v[34:35], v[40:41], 0, v[50:51]
	s_nop 5
	v_add_f32_e32 v30, v42, v30
	v_add_f32_e32 v31, v42, v31
	v_add_f32_e32 v32, v42, v32
	v_add_f32_e32 v33, v42, v33
	s_waitcnt vmcnt(3)
	v_mov_b64_e32 v[34:35], v[220:221]
	v_lshlrev_b32_e32 v36, 16, v34
	v_mul_f32_e32 v37, 0x3d372713, v36
	v_mul_f32_e32 v37, v37, v36
	v_fma_f32 v37, v37, v36, v36
	v_mul_f32_e32 v37, 0xc0135761, v37
	v_exp_f32_e32 v37, v37
	v_and_b32_e32 v34, 0xffff0000, v34
	v_add_f32_e32 v37, 1.0, v37
	v_rcp_f32_e32 v37, v37
	s_nop 0
	v_mul_f32_e32 v36, v37, v36
	v_mul_f32_e32 v30, v30, v36
	v_mul_f32_e32 v36, 0x3d372713, v34
	v_mul_f32_e32 v36, v36, v34
	v_fma_f32 v36, v36, v34, v34
	v_mul_f32_e32 v36, 0xc0135761, v36
	v_exp_f32_e32 v36, v36
	s_nop 0
	v_add_f32_e32 v36, 1.0, v36
	v_rcp_f32_e32 v36, v36
	s_nop 0
	v_mul_f32_e32 v34, v36, v34
	v_mul_f32_e32 v31, v31, v34
	v_cvt_pk_bf16_f32 v30, v30, v31
	v_lshlrev_b32_e32 v31, 16, v35
	v_mul_f32_e32 v34, 0x3d372713, v31
	v_mul_f32_e32 v34, v34, v31
	v_fma_f32 v34, v34, v31, v31
	v_mul_f32_e32 v34, 0xc0135761, v34
	v_exp_f32_e32 v34, v34
	s_nop 0
	v_add_f32_e32 v34, 1.0, v34
	v_rcp_f32_e32 v34, v34
	s_nop 0
	v_mul_f32_e32 v31, v34, v31
	v_mul_f32_e32 v31, v32, v31
	v_and_b32_e32 v32, 0xffff0000, v35
	v_mul_f32_e32 v34, 0x3d372713, v32
	v_mul_f32_e32 v34, v34, v32
	v_fma_f32 v34, v34, v32, v32
	v_mul_f32_e32 v34, 0xc0135761, v34
	v_exp_f32_e32 v34, v34
	s_nop 0
	v_add_f32_e32 v34, 1.0, v34
	v_rcp_f32_e32 v34, v34
	s_nop 0
	v_mul_f32_e32 v32, v34, v32
	v_or_b32_e32 v34, 16, v46
	v_mad_i64_i32 v[36:37], s[10:11], v34, s16, v[56:57]
	v_mul_f32_e32 v32, v33, v32
	v_cvt_pk_bf16_f32 v31, v31, v32
	global_store_dwordx2 v[38:39], v[30:31], off offset:96
	v_lshl_add_u64 v[38:39], v[36:37], 0, s[18:19]
	v_lshl_add_u64 v[44:45], v[38:39], 0, v[54:55]
	global_load_dwordx2 v[44:45], v[44:45], off
	v_lshl_add_u64 v[216:217], v[38:39], 0, v[52:53]
	global_load_dwordx2 v[216:217], v[216:217], off
	v_lshl_add_u64 v[218:219], v[38:39], 0, v[48:49]
	global_load_dwordx2 v[218:219], v[218:219], off
	v_lshl_add_u64 v[220:221], v[38:39], 0, v[50:51]
	global_load_dwordx2 v[220:221], v[220:221], off
	v_ashrrev_i32_e32 v35, 31, v34
	global_load_dwordx4 v[30:33], v[108:109], off
	global_load_dword v42, v[106:107], off offset:64
	v_lshlrev_b64 v[40:41], 10, v[34:35]
	ds_read_b128 v[34:37], v193
	v_lshl_add_u64 v[40:41], v[138:139], 0, v[40:41]
	s_waitcnt vmcnt(1) lgkmcnt(0)
	v_mfma_f32_16x16x32_bf16 v[34:37], v[34:37], v[30:33], 0
	v_lshlrev_b32_e32 v43, 16, v44
	v_mul_f32_e32 v47, 0x3d372713, v43
	v_mul_f32_e32 v47, v47, v43
	v_fma_f32 v47, v47, v43, v43
	v_mul_f32_e32 v47, 0xc0135761, v47
	v_exp_f32_e32 v47, v47
	s_waitcnt vmcnt(0)
	s_nop 0
	v_add_f32_e32 v34, v42, v34
	v_add_f32_e32 v35, v42, v35
	v_add_f32_e32 v36, v42, v36
	v_add_f32_e32 v47, 1.0, v47
	v_rcp_f32_e32 v47, v47
	v_add_f32_e32 v37, v42, v37
	v_mul_f32_e32 v43, v47, v43
	v_mul_f32_e32 v34, v34, v43
	v_and_b32_e32 v43, 0xffff0000, v44
	v_mul_f32_e32 v44, 0x3d372713, v43
	v_mul_f32_e32 v44, v44, v43
	v_fma_f32 v44, v44, v43, v43
	v_mul_f32_e32 v44, 0xc0135761, v44
	v_exp_f32_e32 v44, v44
	s_nop 0
	v_add_f32_e32 v44, 1.0, v44
	v_rcp_f32_e32 v44, v44
	s_nop 0
	v_mul_f32_e32 v43, v44, v43
	v_mul_f32_e32 v35, v35, v43
	v_cvt_pk_bf16_f32 v34, v34, v35
	v_lshlrev_b32_e32 v35, 16, v45
	v_mul_f32_e32 v43, 0x3d372713, v35
	v_mul_f32_e32 v43, v43, v35
	v_fma_f32 v43, v43, v35, v35
	v_mul_f32_e32 v43, 0xc0135761, v43
	v_exp_f32_e32 v43, v43
	s_nop 0
	v_add_f32_e32 v43, 1.0, v43
	v_rcp_f32_e32 v43, v43
	s_nop 0
	v_mul_f32_e32 v35, v43, v35
	v_mul_f32_e32 v35, v36, v35
	v_and_b32_e32 v36, 0xffff0000, v45
	v_mul_f32_e32 v43, 0x3d372713, v36
	v_mul_f32_e32 v43, v43, v36
	v_fma_f32 v43, v43, v36, v36
	v_mul_f32_e32 v43, 0xc0135761, v43
	v_exp_f32_e32 v43, v43
	v_lshl_add_u64 v[44:45], v[38:39], 0, v[52:53]
	v_add_f32_e32 v43, 1.0, v43
	v_rcp_f32_e32 v43, v43
	s_nop 0
	v_mul_f32_e32 v36, v43, v36
	v_mul_f32_e32 v36, v37, v36
	v_cvt_pk_bf16_f32 v35, v35, v36
	s_waitcnt vmcnt(2)
	v_mov_b64_e32 v[44:45], v[216:217]
	v_lshlrev_b32_e32 v43, 16, v44
	global_store_dwordx2 v[40:41], v[34:35], off
	ds_read_b128 v[34:37], v193 offset:4352
	v_mul_f32_e32 v47, 0x3d372713, v43
	v_mul_f32_e32 v47, v47, v43
	v_fma_f32 v47, v47, v43, v43
	v_mul_f32_e32 v47, 0xc0135761, v47
	v_exp_f32_e32 v47, v47
	s_waitcnt lgkmcnt(0)
	v_mfma_f32_16x16x32_bf16 v[34:37], v[34:37], v[30:33], 0
	v_add_f32_e32 v47, 1.0, v47
	v_rcp_f32_e32 v47, v47
	s_nop 5
	v_add_f32_e32 v34, v42, v34
	v_add_f32_e32 v35, v42, v35
	v_mul_f32_e32 v43, v47, v43
	v_mul_f32_e32 v34, v34, v43
	v_and_b32_e32 v43, 0xffff0000, v44
	v_mul_f32_e32 v44, 0x3d372713, v43
	v_mul_f32_e32 v44, v44, v43
	v_fma_f32 v44, v44, v43, v43
	v_mul_f32_e32 v44, 0xc0135761, v44
	v_exp_f32_e32 v44, v44
	v_add_f32_e32 v36, v42, v36
	v_add_f32_e32 v37, v42, v37
	v_add_f32_e32 v44, 1.0, v44
	v_rcp_f32_e32 v44, v44
	s_nop 0
	v_mul_f32_e32 v43, v44, v43
	v_mul_f32_e32 v35, v35, v43
	v_cvt_pk_bf16_f32 v34, v34, v35
	v_lshlrev_b32_e32 v35, 16, v45
	v_mul_f32_e32 v43, 0x3d372713, v35
	v_mul_f32_e32 v43, v43, v35
	v_fma_f32 v43, v43, v35, v35
	v_mul_f32_e32 v43, 0xc0135761, v43
	v_exp_f32_e32 v43, v43
	s_nop 0
	v_add_f32_e32 v43, 1.0, v43
	v_rcp_f32_e32 v43, v43
	s_nop 0
	v_mul_f32_e32 v35, v43, v35
	v_mul_f32_e32 v35, v36, v35
	v_and_b32_e32 v36, 0xffff0000, v45
	v_mul_f32_e32 v43, 0x3d372713, v36
	v_mul_f32_e32 v43, v43, v36
	v_fma_f32 v43, v43, v36, v36
	v_mul_f32_e32 v43, 0xc0135761, v43
	v_exp_f32_e32 v43, v43
	v_lshl_add_u64 v[44:45], v[38:39], 0, v[48:49]
	v_add_f32_e32 v43, 1.0, v43
	v_rcp_f32_e32 v43, v43
	s_nop 0
	v_mul_f32_e32 v36, v43, v36
	v_mul_f32_e32 v36, v37, v36
	v_cvt_pk_bf16_f32 v35, v35, v36
	s_waitcnt vmcnt(2)
	v_mov_b64_e32 v[44:45], v[218:219]
	v_lshlrev_b32_e32 v43, 16, v44
	global_store_dwordx2 v[40:41], v[34:35], off offset:32
	ds_read_b128 v[34:37], v193 offset:8704
	v_mul_f32_e32 v47, 0x3d372713, v43
	v_mul_f32_e32 v47, v47, v43
	v_fma_f32 v47, v47, v43, v43
	v_mul_f32_e32 v47, 0xc0135761, v47
	v_exp_f32_e32 v47, v47
	s_waitcnt lgkmcnt(0)
	v_mfma_f32_16x16x32_bf16 v[34:37], v[34:37], v[30:33], 0
	v_add_f32_e32 v47, 1.0, v47
	v_rcp_f32_e32 v47, v47
	s_nop 5
	v_add_f32_e32 v34, v42, v34
	v_add_f32_e32 v35, v42, v35
	v_mul_f32_e32 v43, v47, v43
	v_mul_f32_e32 v34, v34, v43
	v_and_b32_e32 v43, 0xffff0000, v44
	v_mul_f32_e32 v44, 0x3d372713, v43
	v_mul_f32_e32 v44, v44, v43
	v_fma_f32 v44, v44, v43, v43
	v_mul_f32_e32 v44, 0xc0135761, v44
	v_exp_f32_e32 v44, v44
	v_add_f32_e32 v36, v42, v36
	v_add_f32_e32 v37, v42, v37
	v_add_f32_e32 v44, 1.0, v44
	v_rcp_f32_e32 v44, v44
	s_nop 0
	v_mul_f32_e32 v43, v44, v43
	v_mul_f32_e32 v35, v35, v43
	v_cvt_pk_bf16_f32 v34, v34, v35
	v_lshlrev_b32_e32 v35, 16, v45
	v_mul_f32_e32 v43, 0x3d372713, v35
	v_mul_f32_e32 v43, v43, v35
	v_fma_f32 v43, v43, v35, v35
	v_mul_f32_e32 v43, 0xc0135761, v43
	v_exp_f32_e32 v43, v43
	s_nop 0
	v_add_f32_e32 v43, 1.0, v43
	v_rcp_f32_e32 v43, v43
	s_nop 0
	v_mul_f32_e32 v35, v43, v35
	v_mul_f32_e32 v35, v36, v35
	v_and_b32_e32 v36, 0xffff0000, v45
	v_mul_f32_e32 v43, 0x3d372713, v36
	v_mul_f32_e32 v43, v43, v36
	v_fma_f32 v43, v43, v36, v36
	v_mul_f32_e32 v43, 0xc0135761, v43
	v_exp_f32_e32 v43, v43
	s_nop 0
	v_add_f32_e32 v43, 1.0, v43
	v_rcp_f32_e32 v43, v43
	s_nop 0
	v_mul_f32_e32 v36, v43, v36
	v_mul_f32_e32 v36, v37, v36
	v_cvt_pk_bf16_f32 v35, v35, v36
	global_store_dwordx2 v[40:41], v[34:35], off offset:64
	ds_read_b128 v[34:37], v193 offset:13056
	s_waitcnt lgkmcnt(0)
	v_mfma_f32_16x16x32_bf16 v[30:33], v[34:37], v[30:33], 0
	v_lshl_add_u64 v[34:35], v[38:39], 0, v[50:51]
	v_or_b32_e32 v38, 32, v46
	s_nop 4
	v_add_f32_e32 v30, v42, v30
	v_add_f32_e32 v31, v42, v31
	v_add_f32_e32 v32, v42, v32
	v_add_f32_e32 v33, v42, v33
	v_ashrrev_i32_e32 v39, 31, v38
	v_lshlrev_b64 v[44:45], 10, v[38:39]
	v_lshl_add_u64 v[44:45], v[138:139], 0, v[44:45]
	s_waitcnt vmcnt(3)
	v_mov_b64_e32 v[34:35], v[220:221]
	v_lshlrev_b32_e32 v36, 16, v34
	v_mul_f32_e32 v37, 0x3d372713, v36
	v_mul_f32_e32 v37, v37, v36
	v_fma_f32 v37, v37, v36, v36
	v_mul_f32_e32 v37, 0xc0135761, v37
	v_exp_f32_e32 v37, v37
	v_and_b32_e32 v34, 0xffff0000, v34
	v_add_f32_e32 v37, 1.0, v37
	v_rcp_f32_e32 v37, v37
	s_nop 0
	v_mul_f32_e32 v36, v37, v36
	v_mul_f32_e32 v30, v30, v36
	v_mul_f32_e32 v36, 0x3d372713, v34
	v_mul_f32_e32 v36, v36, v34
	v_fma_f32 v36, v36, v34, v34
	v_mul_f32_e32 v36, 0xc0135761, v36
	v_exp_f32_e32 v36, v36
	s_nop 0
	v_add_f32_e32 v36, 1.0, v36
	v_rcp_f32_e32 v36, v36
	s_nop 0
	v_mul_f32_e32 v34, v36, v34
	v_mul_f32_e32 v31, v31, v34
	v_cvt_pk_bf16_f32 v30, v30, v31
	v_lshlrev_b32_e32 v31, 16, v35
	v_mul_f32_e32 v34, 0x3d372713, v31
	v_mul_f32_e32 v34, v34, v31
	v_fma_f32 v34, v34, v31, v31
	v_mul_f32_e32 v34, 0xc0135761, v34
	v_exp_f32_e32 v34, v34
	s_nop 0
	v_add_f32_e32 v34, 1.0, v34
	v_rcp_f32_e32 v34, v34
	s_nop 0
	v_mul_f32_e32 v31, v34, v31
	v_mul_f32_e32 v31, v32, v31
	v_and_b32_e32 v32, 0xffff0000, v35
	v_mul_f32_e32 v34, 0x3d372713, v32
	v_mul_f32_e32 v34, v34, v32
	v_fma_f32 v34, v34, v32, v32
	v_mul_f32_e32 v34, 0xc0135761, v34
	v_exp_f32_e32 v34, v34
	s_nop 0
	v_add_f32_e32 v34, 1.0, v34
	v_rcp_f32_e32 v34, v34
	s_nop 0
	v_mul_f32_e32 v32, v34, v32
	v_mul_f32_e32 v32, v33, v32
	v_cvt_pk_bf16_f32 v31, v31, v32
	global_store_dwordx2 v[40:41], v[30:31], off offset:96
	global_load_dwordx4 v[34:37], v[110:111], off
	s_nop 0
	global_load_dwordx4 v[30:33], v[112:113], off
	v_mad_i64_i32 v[40:41], s[10:11], v38, s16, v[56:57]
	v_lshl_add_u64 v[42:43], v[40:41], 0, s[18:19]
	ds_read_b128 v[38:41], v193
	ds_read_b128 v[58:61], v193 offset:64
	global_load_dword v47, v[106:107], off offset:128
	s_waitcnt vmcnt(2) lgkmcnt(1)
	v_mfma_f32_16x16x32_bf16 v[38:41], v[38:41], v[34:37], 0
	s_waitcnt vmcnt(1) lgkmcnt(0)
	v_mfma_f32_16x16x32_bf16 v[38:41], v[58:61], v[30:33], v[38:41]
	v_lshl_add_u64 v[58:59], v[42:43], 0, v[54:55]
	global_load_dwordx2 v[58:59], v[58:59], off
	v_lshl_add_u64 v[216:217], v[42:43], 0, v[52:53]
	global_load_dwordx2 v[216:217], v[216:217], off
	v_lshl_add_u64 v[218:219], v[42:43], 0, v[48:49]
	global_load_dwordx2 v[218:219], v[218:219], off
	v_lshl_add_u64 v[220:221], v[42:43], 0, v[50:51]
	global_load_dwordx2 v[220:221], v[220:221], off
	s_waitcnt vmcnt(0)
	v_lshlrev_b32_e32 v60, 16, v58
	v_mul_f32_e32 v61, 0x3d372713, v60
	v_mul_f32_e32 v61, v61, v60
	v_fma_f32 v61, v61, v60, v60
	v_mul_f32_e32 v61, 0xc0135761, v61
	v_exp_f32_e32 v61, v61
	v_add_f32_e32 v38, v47, v38
	v_and_b32_e32 v58, 0xffff0000, v58
	v_add_f32_e32 v39, v47, v39
	v_add_f32_e32 v61, 1.0, v61
	v_rcp_f32_e32 v61, v61
	v_add_f32_e32 v40, v47, v40
	v_add_f32_e32 v41, v47, v41
	v_mul_f32_e32 v60, v61, v60
	v_mul_f32_e32 v38, v38, v60
	v_mul_f32_e32 v60, 0x3d372713, v58
	v_mul_f32_e32 v60, v60, v58
	v_fma_f32 v60, v60, v58, v58
	v_mul_f32_e32 v60, 0xc0135761, v60
	v_exp_f32_e32 v60, v60
	s_nop 0
	v_add_f32_e32 v60, 1.0, v60
	v_rcp_f32_e32 v60, v60
	s_nop 0
	v_mul_f32_e32 v58, v60, v58
	v_mul_f32_e32 v39, v39, v58
	v_cvt_pk_bf16_f32 v38, v38, v39
	v_lshlrev_b32_e32 v39, 16, v59
	v_mul_f32_e32 v58, 0x3d372713, v39
	v_mul_f32_e32 v58, v58, v39
	v_fma_f32 v58, v58, v39, v39
	v_mul_f32_e32 v58, 0xc0135761, v58
	v_exp_f32_e32 v58, v58
	s_nop 0
	v_add_f32_e32 v58, 1.0, v58
	v_rcp_f32_e32 v58, v58
	s_nop 0
	v_mul_f32_e32 v39, v58, v39
	v_mul_f32_e32 v39, v40, v39
	v_and_b32_e32 v40, 0xffff0000, v59
	v_mul_f32_e32 v58, 0x3d372713, v40
	v_mul_f32_e32 v58, v58, v40
	v_fma_f32 v58, v58, v40, v40
	v_mul_f32_e32 v58, 0xc0135761, v58
	v_exp_f32_e32 v58, v58
	s_nop 0
	v_add_f32_e32 v58, 1.0, v58
	v_rcp_f32_e32 v58, v58
	s_nop 0
	v_mul_f32_e32 v40, v58, v40
	v_mul_f32_e32 v40, v41, v40
	v_cvt_pk_bf16_f32 v39, v39, v40
	global_store_dwordx2 v[44:45], v[38:39], off
	ds_read_b128 v[38:41], v193 offset:4352
	ds_read_b128 v[58:61], v193 offset:4416
	s_waitcnt lgkmcnt(1)
	v_mfma_f32_16x16x32_bf16 v[38:41], v[38:41], v[34:37], 0
	s_waitcnt lgkmcnt(0)
	v_mfma_f32_16x16x32_bf16 v[38:41], v[58:61], v[30:33], v[38:41]
	v_lshl_add_u64 v[58:59], v[42:43], 0, v[52:53]
	s_waitcnt vmcnt(2)
	v_mov_b64_e32 v[58:59], v[216:217]
	v_lshlrev_b32_e32 v60, 16, v58
	v_mul_f32_e32 v61, 0x3d372713, v60
	v_mul_f32_e32 v61, v61, v60
	v_fma_f32 v61, v61, v60, v60
	v_mul_f32_e32 v61, 0xc0135761, v61
	v_exp_f32_e32 v61, v61
	v_add_f32_e32 v38, v47, v38
	v_and_b32_e32 v58, 0xffff0000, v58
	v_add_f32_e32 v39, v47, v39
	v_add_f32_e32 v61, 1.0, v61
	v_rcp_f32_e32 v61, v61
	v_add_f32_e32 v40, v47, v40
	v_add_f32_e32 v41, v47, v41
	v_mul_f32_e32 v60, v61, v60
	v_mul_f32_e32 v38, v38, v60
	v_mul_f32_e32 v60, 0x3d372713, v58
	v_mul_f32_e32 v60, v60, v58
	v_fma_f32 v60, v60, v58, v58
	v_mul_f32_e32 v60, 0xc0135761, v60
	v_exp_f32_e32 v60, v60
	s_nop 0
	v_add_f32_e32 v60, 1.0, v60
	v_rcp_f32_e32 v60, v60
	s_nop 0
	v_mul_f32_e32 v58, v60, v58
	v_mul_f32_e32 v39, v39, v58
	v_cvt_pk_bf16_f32 v38, v38, v39
	v_lshlrev_b32_e32 v39, 16, v59
	v_mul_f32_e32 v58, 0x3d372713, v39
	v_mul_f32_e32 v58, v58, v39
	v_fma_f32 v58, v58, v39, v39
	v_mul_f32_e32 v58, 0xc0135761, v58
	v_exp_f32_e32 v58, v58
	s_nop 0
	v_add_f32_e32 v58, 1.0, v58
	v_rcp_f32_e32 v58, v58
	s_nop 0
	v_mul_f32_e32 v39, v58, v39
	v_mul_f32_e32 v39, v40, v39
	v_and_b32_e32 v40, 0xffff0000, v59
	v_mul_f32_e32 v58, 0x3d372713, v40
	v_mul_f32_e32 v58, v58, v40
	v_fma_f32 v58, v58, v40, v40
	v_mul_f32_e32 v58, 0xc0135761, v58
	v_exp_f32_e32 v58, v58
	s_nop 0
	v_add_f32_e32 v58, 1.0, v58
	v_rcp_f32_e32 v58, v58
	s_nop 0
	v_mul_f32_e32 v40, v58, v40
	v_mul_f32_e32 v40, v41, v40
	v_cvt_pk_bf16_f32 v39, v39, v40
	global_store_dwordx2 v[44:45], v[38:39], off offset:32
	ds_read_b128 v[38:41], v193 offset:8704
	ds_read_b128 v[58:61], v193 offset:8768
	s_waitcnt lgkmcnt(1)
	v_mfma_f32_16x16x32_bf16 v[38:41], v[38:41], v[34:37], 0
	s_waitcnt lgkmcnt(0)
	v_mfma_f32_16x16x32_bf16 v[38:41], v[58:61], v[30:33], v[38:41]
	v_lshl_add_u64 v[58:59], v[42:43], 0, v[48:49]
	s_waitcnt vmcnt(2)
	v_mov_b64_e32 v[58:59], v[218:219]
	v_lshlrev_b32_e32 v60, 16, v58
	v_mul_f32_e32 v61, 0x3d372713, v60
	v_mul_f32_e32 v61, v61, v60
	v_fma_f32 v61, v61, v60, v60
	v_mul_f32_e32 v61, 0xc0135761, v61
	v_exp_f32_e32 v61, v61
	v_add_f32_e32 v38, v47, v38
	v_and_b32_e32 v58, 0xffff0000, v58
	v_add_f32_e32 v39, v47, v39
	v_add_f32_e32 v61, 1.0, v61
	v_rcp_f32_e32 v61, v61
	v_add_f32_e32 v40, v47, v40
	v_add_f32_e32 v41, v47, v41
	v_mul_f32_e32 v60, v61, v60
	v_mul_f32_e32 v38, v38, v60
	v_mul_f32_e32 v60, 0x3d372713, v58
	v_mul_f32_e32 v60, v60, v58
	v_fma_f32 v60, v60, v58, v58
	v_mul_f32_e32 v60, 0xc0135761, v60
	v_exp_f32_e32 v60, v60
	s_nop 0
	v_add_f32_e32 v60, 1.0, v60
	v_rcp_f32_e32 v60, v60
	s_nop 0
	v_mul_f32_e32 v58, v60, v58
	v_mul_f32_e32 v39, v39, v58
	v_cvt_pk_bf16_f32 v38, v38, v39
	v_lshlrev_b32_e32 v39, 16, v59
	v_mul_f32_e32 v58, 0x3d372713, v39
	v_mul_f32_e32 v58, v58, v39
	v_fma_f32 v58, v58, v39, v39
	v_mul_f32_e32 v58, 0xc0135761, v58
	v_exp_f32_e32 v58, v58
	s_nop 0
	v_add_f32_e32 v58, 1.0, v58
	v_rcp_f32_e32 v58, v58
	s_nop 0
	v_mul_f32_e32 v39, v58, v39
	v_mul_f32_e32 v39, v40, v39
	v_and_b32_e32 v40, 0xffff0000, v59
	v_mul_f32_e32 v58, 0x3d372713, v40
	v_mul_f32_e32 v58, v58, v40
	v_fma_f32 v58, v58, v40, v40
	v_mul_f32_e32 v58, 0xc0135761, v58
	v_exp_f32_e32 v58, v58
	s_nop 0
	v_add_f32_e32 v58, 1.0, v58
	v_rcp_f32_e32 v58, v58
	s_nop 0
	v_mul_f32_e32 v40, v58, v40
	v_mul_f32_e32 v40, v41, v40
	v_cvt_pk_bf16_f32 v39, v39, v40
	global_store_dwordx2 v[44:45], v[38:39], off offset:64
	ds_read_b128 v[38:41], v193 offset:13056
	s_waitcnt lgkmcnt(0)
	v_mfma_f32_16x16x32_bf16 v[34:37], v[38:41], v[34:37], 0
	ds_read_b128 v[38:41], v193 offset:13120
	s_waitcnt lgkmcnt(0)
	v_mfma_f32_16x16x32_bf16 v[30:33], v[38:41], v[30:33], v[34:37]
	s_nop 4
	v_lshl_add_u64 v[34:35], v[42:43], 0, v[50:51]
	v_or_b32_e32 v38, 48, v46
	v_add_f32_e32 v30, v47, v30
	v_add_f32_e32 v31, v47, v31
	v_add_f32_e32 v32, v47, v32
	v_add_f32_e32 v33, v47, v33
	v_ashrrev_i32_e32 v39, 31, v38
	v_mad_i64_i32 v[40:41], s[10:11], v38, s16, v[56:57]
	v_lshl_add_u64 v[42:43], v[40:41], 0, s[18:19]
	s_waitcnt vmcnt(3)
	v_mov_b64_e32 v[34:35], v[220:221]
	v_lshlrev_b32_e32 v36, 16, v34
	v_mul_f32_e32 v37, 0x3d372713, v36
	v_mul_f32_e32 v37, v37, v36
	v_fma_f32 v37, v37, v36, v36
	v_mul_f32_e32 v37, 0xc0135761, v37
	v_exp_f32_e32 v37, v37
	v_and_b32_e32 v34, 0xffff0000, v34
	v_add_f32_e32 v37, 1.0, v37
	v_rcp_f32_e32 v37, v37
	s_nop 0
	v_mul_f32_e32 v36, v37, v36
	v_mul_f32_e32 v30, v30, v36
	v_mul_f32_e32 v36, 0x3d372713, v34
	v_mul_f32_e32 v36, v36, v34
	v_fma_f32 v36, v36, v34, v34
	v_mul_f32_e32 v36, 0xc0135761, v36
	v_exp_f32_e32 v36, v36
	s_nop 0
	v_add_f32_e32 v36, 1.0, v36
	v_rcp_f32_e32 v36, v36
	s_nop 0
	v_mul_f32_e32 v34, v36, v34
	v_mul_f32_e32 v31, v31, v34
	v_cvt_pk_bf16_f32 v30, v30, v31
	v_lshlrev_b32_e32 v31, 16, v35
	v_mul_f32_e32 v34, 0x3d372713, v31
	v_mul_f32_e32 v34, v34, v31
	v_fma_f32 v34, v34, v31, v31
	v_mul_f32_e32 v34, 0xc0135761, v34
	v_exp_f32_e32 v34, v34
	s_nop 0
	v_add_f32_e32 v34, 1.0, v34
	v_rcp_f32_e32 v34, v34
	s_nop 0
	v_mul_f32_e32 v31, v34, v31
	v_mul_f32_e32 v31, v32, v31
	v_and_b32_e32 v32, 0xffff0000, v35
	v_mul_f32_e32 v34, 0x3d372713, v32
	v_mul_f32_e32 v34, v34, v32
	v_fma_f32 v34, v34, v32, v32
	v_mul_f32_e32 v34, 0xc0135761, v34
	v_exp_f32_e32 v34, v34
	s_nop 0
	v_add_f32_e32 v34, 1.0, v34
	v_rcp_f32_e32 v34, v34
	s_nop 0
	v_mul_f32_e32 v32, v34, v32
	v_mul_f32_e32 v32, v33, v32
	v_cvt_pk_bf16_f32 v31, v31, v32
	global_store_dwordx2 v[44:45], v[30:31], off offset:96
	global_load_dwordx4 v[34:37], v[114:115], off
	s_nop 0
	global_load_dwordx4 v[30:33], v[116:117], off
	v_lshlrev_b64 v[44:45], 10, v[38:39]
	ds_read_b128 v[38:41], v193
	ds_read_b128 v[58:61], v193 offset:64
	s_waitcnt vmcnt(1) lgkmcnt(1)
	v_mfma_f32_16x16x32_bf16 v[38:41], v[38:41], v[34:37], 0
	global_load_dword v47, v[106:107], off offset:192
	v_lshl_add_u64 v[44:45], v[138:139], 0, v[44:45]
	s_waitcnt vmcnt(1) lgkmcnt(0)
	v_mfma_f32_16x16x32_bf16 v[38:41], v[58:61], v[30:33], v[38:41]
	v_lshl_add_u64 v[58:59], v[42:43], 0, v[54:55]
	global_load_dwordx2 v[58:59], v[58:59], off
	v_lshl_add_u64 v[216:217], v[42:43], 0, v[52:53]
	global_load_dwordx2 v[216:217], v[216:217], off
	v_lshl_add_u64 v[218:219], v[42:43], 0, v[48:49]
	global_load_dwordx2 v[218:219], v[218:219], off
	v_lshl_add_u64 v[220:221], v[42:43], 0, v[50:51]
	global_load_dwordx2 v[220:221], v[220:221], off
	s_waitcnt vmcnt(0)
	v_lshlrev_b32_e32 v60, 16, v58
	v_mul_f32_e32 v61, 0x3d372713, v60
	v_mul_f32_e32 v61, v61, v60
	v_fma_f32 v61, v61, v60, v60
	v_mul_f32_e32 v61, 0xc0135761, v61
	v_exp_f32_e32 v61, v61
	v_add_f32_e32 v38, v47, v38
	v_and_b32_e32 v58, 0xffff0000, v58
	v_add_f32_e32 v39, v47, v39
	v_add_f32_e32 v61, 1.0, v61
	v_rcp_f32_e32 v61, v61
	v_add_f32_e32 v40, v47, v40
	v_add_f32_e32 v41, v47, v41
	v_mul_f32_e32 v60, v61, v60
	v_mul_f32_e32 v38, v38, v60
	v_mul_f32_e32 v60, 0x3d372713, v58
	v_mul_f32_e32 v60, v60, v58
	v_fma_f32 v60, v60, v58, v58
	v_mul_f32_e32 v60, 0xc0135761, v60
	v_exp_f32_e32 v60, v60
	s_nop 0
	v_add_f32_e32 v60, 1.0, v60
	v_rcp_f32_e32 v60, v60
	s_nop 0
	v_mul_f32_e32 v58, v60, v58
	v_mul_f32_e32 v39, v39, v58
	v_cvt_pk_bf16_f32 v38, v38, v39
	v_lshlrev_b32_e32 v39, 16, v59
	v_mul_f32_e32 v58, 0x3d372713, v39
	v_mul_f32_e32 v58, v58, v39
	v_fma_f32 v58, v58, v39, v39
	v_mul_f32_e32 v58, 0xc0135761, v58
	v_exp_f32_e32 v58, v58
	s_nop 0
	v_add_f32_e32 v58, 1.0, v58
	v_rcp_f32_e32 v58, v58
	s_nop 0
	v_mul_f32_e32 v39, v58, v39
	v_mul_f32_e32 v39, v40, v39
	v_and_b32_e32 v40, 0xffff0000, v59
	v_mul_f32_e32 v58, 0x3d372713, v40
	v_mul_f32_e32 v58, v58, v40
	v_fma_f32 v58, v58, v40, v40
	v_mul_f32_e32 v58, 0xc0135761, v58
	v_exp_f32_e32 v58, v58
	s_nop 0
	v_add_f32_e32 v58, 1.0, v58
	v_rcp_f32_e32 v58, v58
	s_nop 0
	v_mul_f32_e32 v40, v58, v40
	v_mul_f32_e32 v40, v41, v40
	v_cvt_pk_bf16_f32 v39, v39, v40
	global_store_dwordx2 v[44:45], v[38:39], off
	ds_read_b128 v[38:41], v193 offset:4352
	ds_read_b128 v[58:61], v193 offset:4416
	s_waitcnt lgkmcnt(1)
	v_mfma_f32_16x16x32_bf16 v[38:41], v[38:41], v[34:37], 0
	s_waitcnt lgkmcnt(0)
	v_mfma_f32_16x16x32_bf16 v[38:41], v[58:61], v[30:33], v[38:41]
	v_lshl_add_u64 v[58:59], v[42:43], 0, v[52:53]
	s_waitcnt vmcnt(2)
	v_mov_b64_e32 v[58:59], v[216:217]
	v_lshlrev_b32_e32 v60, 16, v58
	v_mul_f32_e32 v61, 0x3d372713, v60
	v_mul_f32_e32 v61, v61, v60
	v_fma_f32 v61, v61, v60, v60
	v_mul_f32_e32 v61, 0xc0135761, v61
	v_exp_f32_e32 v61, v61
	v_add_f32_e32 v38, v47, v38
	v_and_b32_e32 v58, 0xffff0000, v58
	v_add_f32_e32 v39, v47, v39
	v_add_f32_e32 v61, 1.0, v61
	v_rcp_f32_e32 v61, v61
	v_add_f32_e32 v40, v47, v40
	v_add_f32_e32 v41, v47, v41
	v_mul_f32_e32 v60, v61, v60
	v_mul_f32_e32 v38, v38, v60
	v_mul_f32_e32 v60, 0x3d372713, v58
	v_mul_f32_e32 v60, v60, v58
	v_fma_f32 v60, v60, v58, v58
	v_mul_f32_e32 v60, 0xc0135761, v60
	v_exp_f32_e32 v60, v60
	s_nop 0
	v_add_f32_e32 v60, 1.0, v60
	v_rcp_f32_e32 v60, v60
	s_nop 0
	v_mul_f32_e32 v58, v60, v58
	v_mul_f32_e32 v39, v39, v58
	v_cvt_pk_bf16_f32 v38, v38, v39
	v_lshlrev_b32_e32 v39, 16, v59
	v_mul_f32_e32 v58, 0x3d372713, v39
	v_mul_f32_e32 v58, v58, v39
	v_fma_f32 v58, v58, v39, v39
	v_mul_f32_e32 v58, 0xc0135761, v58
	v_exp_f32_e32 v58, v58
	s_nop 0
	v_add_f32_e32 v58, 1.0, v58
	v_rcp_f32_e32 v58, v58
	s_nop 0
	v_mul_f32_e32 v39, v58, v39
	v_mul_f32_e32 v39, v40, v39
	v_and_b32_e32 v40, 0xffff0000, v59
	v_mul_f32_e32 v58, 0x3d372713, v40
	v_mul_f32_e32 v58, v58, v40
	v_fma_f32 v58, v58, v40, v40
	v_mul_f32_e32 v58, 0xc0135761, v58
	v_exp_f32_e32 v58, v58
	s_nop 0
	v_add_f32_e32 v58, 1.0, v58
	v_rcp_f32_e32 v58, v58
	s_nop 0
	v_mul_f32_e32 v40, v58, v40
	v_mul_f32_e32 v40, v41, v40
	v_cvt_pk_bf16_f32 v39, v39, v40
	global_store_dwordx2 v[44:45], v[38:39], off offset:32
	ds_read_b128 v[38:41], v193 offset:8704
	ds_read_b128 v[58:61], v193 offset:8768
	s_waitcnt lgkmcnt(1)
	v_mfma_f32_16x16x32_bf16 v[38:41], v[38:41], v[34:37], 0
	s_waitcnt lgkmcnt(0)
	v_mfma_f32_16x16x32_bf16 v[38:41], v[58:61], v[30:33], v[38:41]
	v_lshl_add_u64 v[58:59], v[42:43], 0, v[48:49]
	s_waitcnt vmcnt(2)
	v_mov_b64_e32 v[58:59], v[218:219]
	v_lshlrev_b32_e32 v60, 16, v58
	v_mul_f32_e32 v61, 0x3d372713, v60
	v_mul_f32_e32 v61, v61, v60
	v_fma_f32 v61, v61, v60, v60
	v_mul_f32_e32 v61, 0xc0135761, v61
	v_exp_f32_e32 v61, v61
	v_add_f32_e32 v38, v47, v38
	v_and_b32_e32 v58, 0xffff0000, v58
	v_add_f32_e32 v39, v47, v39
	v_add_f32_e32 v61, 1.0, v61
	v_rcp_f32_e32 v61, v61
	v_add_f32_e32 v40, v47, v40
	v_add_f32_e32 v41, v47, v41
	v_mul_f32_e32 v60, v61, v60
	v_mul_f32_e32 v38, v38, v60
	v_mul_f32_e32 v60, 0x3d372713, v58
	v_mul_f32_e32 v60, v60, v58
	v_fma_f32 v60, v60, v58, v58
	v_mul_f32_e32 v60, 0xc0135761, v60
	v_exp_f32_e32 v60, v60
	s_nop 0
	v_add_f32_e32 v60, 1.0, v60
	v_rcp_f32_e32 v60, v60
	s_nop 0
	v_mul_f32_e32 v58, v60, v58
	v_mul_f32_e32 v39, v39, v58
	v_cvt_pk_bf16_f32 v38, v38, v39
	v_lshlrev_b32_e32 v39, 16, v59
	v_mul_f32_e32 v58, 0x3d372713, v39
	v_mul_f32_e32 v58, v58, v39
	v_fma_f32 v58, v58, v39, v39
	v_mul_f32_e32 v58, 0xc0135761, v58
	v_exp_f32_e32 v58, v58
	s_nop 0
	v_add_f32_e32 v58, 1.0, v58
	v_rcp_f32_e32 v58, v58
	s_nop 0
	v_mul_f32_e32 v39, v58, v39
	v_mul_f32_e32 v39, v40, v39
	v_and_b32_e32 v40, 0xffff0000, v59
	v_mul_f32_e32 v58, 0x3d372713, v40
	v_mul_f32_e32 v58, v58, v40
	v_fma_f32 v58, v58, v40, v40
	v_mul_f32_e32 v58, 0xc0135761, v58
	v_exp_f32_e32 v58, v58
	s_nop 0
	v_add_f32_e32 v58, 1.0, v58
	v_rcp_f32_e32 v58, v58
	s_nop 0
	v_mul_f32_e32 v40, v58, v40
	v_mul_f32_e32 v40, v41, v40
	v_cvt_pk_bf16_f32 v39, v39, v40
	global_store_dwordx2 v[44:45], v[38:39], off offset:64
	ds_read_b128 v[38:41], v193 offset:13056
	s_waitcnt lgkmcnt(0)
	v_mfma_f32_16x16x32_bf16 v[34:37], v[38:41], v[34:37], 0
	ds_read_b128 v[38:41], v193 offset:13120
	s_waitcnt lgkmcnt(0)
	v_mfma_f32_16x16x32_bf16 v[30:33], v[38:41], v[30:33], v[34:37]
	s_nop 4
	v_lshl_add_u64 v[34:35], v[42:43], 0, v[50:51]
	v_or_b32_e32 v42, 64, v46
	v_add_f32_e32 v30, v47, v30
	v_add_f32_e32 v31, v47, v31
	v_add_f32_e32 v32, v47, v32
	v_add_f32_e32 v33, v47, v33
	v_ashrrev_i32_e32 v43, 31, v42
	v_lshlrev_b64 v[60:61], 10, v[42:43]
	v_lshl_add_u64 v[60:61], v[138:139], 0, v[60:61]
	s_waitcnt vmcnt(3)
	v_mov_b64_e32 v[34:35], v[220:221]
	v_lshlrev_b32_e32 v36, 16, v34
	v_mul_f32_e32 v37, 0x3d372713, v36
	v_mul_f32_e32 v37, v37, v36
	v_fma_f32 v37, v37, v36, v36
	v_mul_f32_e32 v37, 0xc0135761, v37
	v_exp_f32_e32 v37, v37
	v_and_b32_e32 v34, 0xffff0000, v34
	v_add_f32_e32 v37, 1.0, v37
	v_rcp_f32_e32 v37, v37
	s_nop 0
	v_mul_f32_e32 v36, v37, v36
	v_mul_f32_e32 v30, v30, v36
	v_mul_f32_e32 v36, 0x3d372713, v34
	v_mul_f32_e32 v36, v36, v34
	v_fma_f32 v36, v36, v34, v34
	v_mul_f32_e32 v36, 0xc0135761, v36
	v_exp_f32_e32 v36, v36
	s_nop 0
	v_add_f32_e32 v36, 1.0, v36
	v_rcp_f32_e32 v36, v36
	s_nop 0
	v_mul_f32_e32 v34, v36, v34
	v_mul_f32_e32 v31, v31, v34
	v_cvt_pk_bf16_f32 v30, v30, v31
	v_lshlrev_b32_e32 v31, 16, v35
	v_mul_f32_e32 v34, 0x3d372713, v31
	v_mul_f32_e32 v34, v34, v31
	v_fma_f32 v34, v34, v31, v31
	v_mul_f32_e32 v34, 0xc0135761, v34
	v_exp_f32_e32 v34, v34
	s_nop 0
	v_add_f32_e32 v34, 1.0, v34
	v_rcp_f32_e32 v34, v34
	s_nop 0
	v_mul_f32_e32 v31, v34, v31
	v_mul_f32_e32 v31, v32, v31
	v_and_b32_e32 v32, 0xffff0000, v35
	v_mul_f32_e32 v34, 0x3d372713, v32
	v_mul_f32_e32 v34, v34, v32
	v_fma_f32 v34, v34, v32, v32
	v_mul_f32_e32 v34, 0xc0135761, v34
	v_exp_f32_e32 v34, v34
	s_nop 0
	v_add_f32_e32 v34, 1.0, v34
	v_rcp_f32_e32 v34, v34
	s_nop 0
	v_mul_f32_e32 v32, v34, v32
	v_mul_f32_e32 v32, v33, v32
	v_cvt_pk_bf16_f32 v31, v31, v32
	global_store_dwordx2 v[44:45], v[30:31], off offset:96
	global_load_dwordx4 v[38:41], v[118:119], off
	global_load_dwordx4 v[34:37], v[120:121], off
	s_nop 0
	global_load_dwordx4 v[30:33], v[122:123], off
	v_mad_i64_i32 v[44:45], s[10:11], v42, s16, v[56:57]
	v_lshl_add_u64 v[58:59], v[44:45], 0, s[18:19]
	ds_read_b128 v[42:45], v193
	ds_read_b128 v[62:65], v193 offset:64
	s_waitcnt vmcnt(2) lgkmcnt(1)
	v_mfma_f32_16x16x32_bf16 v[42:45], v[42:45], v[38:41], 0
	global_load_dword v47, v[106:107], off offset:256
	s_waitcnt vmcnt(2) lgkmcnt(0)
	v_mfma_f32_16x16x32_bf16 v[42:45], v[62:65], v[34:37], v[42:45]
	ds_read_b128 v[62:65], v193 offset:128
	s_waitcnt vmcnt(1) lgkmcnt(0)
	v_mfma_f32_16x16x32_bf16 v[42:45], v[62:65], v[30:33], v[42:45]
	v_lshl_add_u64 v[62:63], v[58:59], 0, v[54:55]
	global_load_dwordx2 v[62:63], v[62:63], off
	v_lshl_add_u64 v[216:217], v[58:59], 0, v[52:53]
	global_load_dwordx2 v[216:217], v[216:217], off
	v_lshl_add_u64 v[218:219], v[58:59], 0, v[48:49]
	global_load_dwordx2 v[218:219], v[218:219], off
	v_lshl_add_u64 v[220:221], v[58:59], 0, v[50:51]
	global_load_dwordx2 v[220:221], v[220:221], off
	s_waitcnt vmcnt(1)
	s_nop 4
	v_add_f32_e32 v42, v47, v42
	v_add_f32_e32 v43, v47, v43
	v_add_f32_e32 v44, v47, v44
	v_add_f32_e32 v45, v47, v45
	s_waitcnt vmcnt(0)
	v_lshlrev_b32_e32 v64, 16, v62
	v_mul_f32_e32 v65, 0x3d372713, v64
	v_mul_f32_e32 v65, v65, v64
	v_fma_f32 v65, v65, v64, v64
	v_mul_f32_e32 v65, 0xc0135761, v65
	v_exp_f32_e32 v65, v65
	v_and_b32_e32 v62, 0xffff0000, v62
	v_add_f32_e32 v65, 1.0, v65
	v_rcp_f32_e32 v65, v65
	s_nop 0
	v_mul_f32_e32 v64, v65, v64
	v_mul_f32_e32 v42, v42, v64
	v_mul_f32_e32 v64, 0x3d372713, v62
	v_mul_f32_e32 v64, v64, v62
	v_fma_f32 v64, v64, v62, v62
	v_mul_f32_e32 v64, 0xc0135761, v64
	v_exp_f32_e32 v64, v64
	s_nop 0
	v_add_f32_e32 v64, 1.0, v64
	v_rcp_f32_e32 v64, v64
	s_nop 0
	v_mul_f32_e32 v62, v64, v62
	v_mul_f32_e32 v43, v43, v62
	v_cvt_pk_bf16_f32 v42, v42, v43
	v_lshlrev_b32_e32 v43, 16, v63
	v_mul_f32_e32 v62, 0x3d372713, v43
	v_mul_f32_e32 v62, v62, v43
	v_fma_f32 v62, v62, v43, v43
	v_mul_f32_e32 v62, 0xc0135761, v62
	v_exp_f32_e32 v62, v62
	s_nop 0
	v_add_f32_e32 v62, 1.0, v62
	v_rcp_f32_e32 v62, v62
	s_nop 0
	v_mul_f32_e32 v43, v62, v43
	v_mul_f32_e32 v43, v44, v43
	v_and_b32_e32 v44, 0xffff0000, v63
	v_mul_f32_e32 v62, 0x3d372713, v44
	v_mul_f32_e32 v62, v62, v44
	v_fma_f32 v62, v62, v44, v44
	v_mul_f32_e32 v62, 0xc0135761, v62
	v_exp_f32_e32 v62, v62
	s_nop 0
	v_add_f32_e32 v62, 1.0, v62
	v_rcp_f32_e32 v62, v62
	s_nop 0
	v_mul_f32_e32 v44, v62, v44
	v_mul_f32_e32 v44, v45, v44
	v_cvt_pk_bf16_f32 v43, v43, v44
	global_store_dwordx2 v[60:61], v[42:43], off
	ds_read_b128 v[42:45], v193 offset:4352
	ds_read_b128 v[62:65], v193 offset:4416
	s_waitcnt lgkmcnt(1)
	v_mfma_f32_16x16x32_bf16 v[42:45], v[42:45], v[38:41], 0
	s_waitcnt lgkmcnt(0)
	v_mfma_f32_16x16x32_bf16 v[42:45], v[62:65], v[34:37], v[42:45]
	ds_read_b128 v[62:65], v193 offset:4480
	s_waitcnt lgkmcnt(0)
	v_mfma_f32_16x16x32_bf16 v[42:45], v[62:65], v[30:33], v[42:45]
	v_lshl_add_u64 v[62:63], v[58:59], 0, v[52:53]
	s_nop 5
	v_add_f32_e32 v42, v47, v42
	v_add_f32_e32 v43, v47, v43
	v_add_f32_e32 v44, v47, v44
	v_add_f32_e32 v45, v47, v45
	s_waitcnt vmcnt(2)
	v_mov_b64_e32 v[62:63], v[216:217]
	v_lshlrev_b32_e32 v64, 16, v62
	v_mul_f32_e32 v65, 0x3d372713, v64
	v_mul_f32_e32 v65, v65, v64
	v_fma_f32 v65, v65, v64, v64
	v_mul_f32_e32 v65, 0xc0135761, v65
	v_exp_f32_e32 v65, v65
	v_and_b32_e32 v62, 0xffff0000, v62
	v_add_f32_e32 v65, 1.0, v65
	v_rcp_f32_e32 v65, v65
	s_nop 0
	v_mul_f32_e32 v64, v65, v64
	v_mul_f32_e32 v42, v42, v64
	v_mul_f32_e32 v64, 0x3d372713, v62
	v_mul_f32_e32 v64, v64, v62
	v_fma_f32 v64, v64, v62, v62
	v_mul_f32_e32 v64, 0xc0135761, v64
	v_exp_f32_e32 v64, v64
	s_nop 0
	v_add_f32_e32 v64, 1.0, v64
	v_rcp_f32_e32 v64, v64
	s_nop 0
	v_mul_f32_e32 v62, v64, v62
	v_mul_f32_e32 v43, v43, v62
	v_cvt_pk_bf16_f32 v42, v42, v43
	v_lshlrev_b32_e32 v43, 16, v63
	v_mul_f32_e32 v62, 0x3d372713, v43
	v_mul_f32_e32 v62, v62, v43
	v_fma_f32 v62, v62, v43, v43
	v_mul_f32_e32 v62, 0xc0135761, v62
	v_exp_f32_e32 v62, v62
	s_nop 0
	v_add_f32_e32 v62, 1.0, v62
	v_rcp_f32_e32 v62, v62
	s_nop 0
	v_mul_f32_e32 v43, v62, v43
	v_mul_f32_e32 v43, v44, v43
	v_and_b32_e32 v44, 0xffff0000, v63
	v_mul_f32_e32 v62, 0x3d372713, v44
	v_mul_f32_e32 v62, v62, v44
	v_fma_f32 v62, v62, v44, v44
	v_mul_f32_e32 v62, 0xc0135761, v62
	v_exp_f32_e32 v62, v62
	s_nop 0
	v_add_f32_e32 v62, 1.0, v62
	v_rcp_f32_e32 v62, v62
	s_nop 0
	v_mul_f32_e32 v44, v62, v44
	v_mul_f32_e32 v44, v45, v44
	v_cvt_pk_bf16_f32 v43, v43, v44
	global_store_dwordx2 v[60:61], v[42:43], off offset:32
	ds_read_b128 v[42:45], v193 offset:8704
	ds_read_b128 v[62:65], v193 offset:8768
	s_waitcnt lgkmcnt(1)
	v_mfma_f32_16x16x32_bf16 v[42:45], v[42:45], v[38:41], 0
	s_waitcnt lgkmcnt(0)
	v_mfma_f32_16x16x32_bf16 v[42:45], v[62:65], v[34:37], v[42:45]
	ds_read_b128 v[62:65], v193 offset:8832
	s_waitcnt lgkmcnt(0)
	v_mfma_f32_16x16x32_bf16 v[42:45], v[62:65], v[30:33], v[42:45]
	v_lshl_add_u64 v[62:63], v[58:59], 0, v[48:49]
	s_nop 5
	v_add_f32_e32 v42, v47, v42
	v_add_f32_e32 v43, v47, v43
	v_add_f32_e32 v44, v47, v44
	v_add_f32_e32 v45, v47, v45
	s_waitcnt vmcnt(2)
	v_mov_b64_e32 v[62:63], v[218:219]
	v_lshlrev_b32_e32 v64, 16, v62
	v_mul_f32_e32 v65, 0x3d372713, v64
	v_mul_f32_e32 v65, v65, v64
	v_fma_f32 v65, v65, v64, v64
	v_mul_f32_e32 v65, 0xc0135761, v65
	v_exp_f32_e32 v65, v65
	v_and_b32_e32 v62, 0xffff0000, v62
	v_add_f32_e32 v65, 1.0, v65
	v_rcp_f32_e32 v65, v65
	s_nop 0
	v_mul_f32_e32 v64, v65, v64
	v_mul_f32_e32 v42, v42, v64
	v_mul_f32_e32 v64, 0x3d372713, v62
	v_mul_f32_e32 v64, v64, v62
	v_fma_f32 v64, v64, v62, v62
	v_mul_f32_e32 v64, 0xc0135761, v64
	v_exp_f32_e32 v64, v64
	s_nop 0
	v_add_f32_e32 v64, 1.0, v64
	v_rcp_f32_e32 v64, v64
	s_nop 0
	v_mul_f32_e32 v62, v64, v62
	v_mul_f32_e32 v43, v43, v62
	v_cvt_pk_bf16_f32 v42, v42, v43
	v_lshlrev_b32_e32 v43, 16, v63
	v_mul_f32_e32 v62, 0x3d372713, v43
	v_mul_f32_e32 v62, v62, v43
	v_fma_f32 v62, v62, v43, v43
	v_mul_f32_e32 v62, 0xc0135761, v62
	v_exp_f32_e32 v62, v62
	s_nop 0
	v_add_f32_e32 v62, 1.0, v62
	v_rcp_f32_e32 v62, v62
	s_nop 0
	v_mul_f32_e32 v43, v62, v43
	v_mul_f32_e32 v43, v44, v43
	v_and_b32_e32 v44, 0xffff0000, v63
	v_mul_f32_e32 v62, 0x3d372713, v44
	v_mul_f32_e32 v62, v62, v44
	v_fma_f32 v62, v62, v44, v44
	v_mul_f32_e32 v62, 0xc0135761, v62
	v_exp_f32_e32 v62, v62
	s_nop 0
	v_add_f32_e32 v62, 1.0, v62
	v_rcp_f32_e32 v62, v62
	s_nop 0
	v_mul_f32_e32 v44, v62, v44
	v_mul_f32_e32 v44, v45, v44
	v_cvt_pk_bf16_f32 v43, v43, v44
	global_store_dwordx2 v[60:61], v[42:43], off offset:64
	ds_read_b128 v[42:45], v193 offset:13056
	s_waitcnt lgkmcnt(0)
	v_mfma_f32_16x16x32_bf16 v[38:41], v[42:45], v[38:41], 0
	ds_read_b128 v[42:45], v193 offset:13120
	s_waitcnt lgkmcnt(0)
	v_mfma_f32_16x16x32_bf16 v[34:37], v[42:45], v[34:37], v[38:41]
	s_nop 4
	ds_read_b128 v[38:41], v193 offset:13184
	v_or_b32_e32 v42, 0x50, v46
	v_mad_i64_i32 v[44:45], s[10:11], v42, s16, v[56:57]
	s_waitcnt lgkmcnt(0)
	v_mfma_f32_16x16x32_bf16 v[30:33], v[38:41], v[30:33], v[34:37]
	s_nop 2
	v_lshl_add_u64 v[34:35], v[58:59], 0, v[50:51]
	v_lshl_add_u64 v[56:57], v[44:45], 0, s[18:19]
	s_nop 1
	v_add_f32_e32 v30, v47, v30
	v_add_f32_e32 v31, v47, v31
	v_add_f32_e32 v32, v47, v32
	v_add_f32_e32 v33, v47, v33
	v_lshl_add_u64 v[54:55], v[56:57], 0, v[54:55]
	v_ashrrev_i32_e32 v43, 31, v42
	v_lshlrev_b64 v[58:59], 10, v[42:43]
	v_lshl_add_u64 v[52:53], v[56:57], 0, v[52:53]
	v_lshl_add_u64 v[48:49], v[56:57], 0, v[48:49]
	s_mov_b64 s[10:11], 0
	s_waitcnt vmcnt(3)
	v_mov_b64_e32 v[34:35], v[220:221]
	v_lshlrev_b32_e32 v36, 16, v34
	v_mul_f32_e32 v37, 0x3d372713, v36
	v_mul_f32_e32 v37, v37, v36
	v_fma_f32 v37, v37, v36, v36
	v_mul_f32_e32 v37, 0xc0135761, v37
	v_exp_f32_e32 v37, v37
	v_and_b32_e32 v34, 0xffff0000, v34
	v_add_f32_e32 v37, 1.0, v37
	v_rcp_f32_e32 v37, v37
	s_nop 0
	v_mul_f32_e32 v36, v37, v36
	v_mul_f32_e32 v30, v30, v36
	v_mul_f32_e32 v36, 0x3d372713, v34
	v_mul_f32_e32 v36, v36, v34
	v_fma_f32 v36, v36, v34, v34
	v_mul_f32_e32 v36, 0xc0135761, v36
	v_exp_f32_e32 v36, v36
	s_nop 0
	v_add_f32_e32 v36, 1.0, v36
	v_rcp_f32_e32 v36, v36
	s_nop 0
	v_mul_f32_e32 v34, v36, v34
	v_mul_f32_e32 v31, v31, v34
	v_cvt_pk_bf16_f32 v30, v30, v31
	v_lshlrev_b32_e32 v31, 16, v35
	v_mul_f32_e32 v34, 0x3d372713, v31
	v_mul_f32_e32 v34, v34, v31
	v_fma_f32 v34, v34, v31, v31
	v_mul_f32_e32 v34, 0xc0135761, v34
	v_exp_f32_e32 v34, v34
	s_nop 0
	v_add_f32_e32 v34, 1.0, v34
	v_rcp_f32_e32 v34, v34
	s_nop 0
	v_mul_f32_e32 v31, v34, v31
	v_mul_f32_e32 v31, v32, v31
	v_and_b32_e32 v32, 0xffff0000, v35
	v_mul_f32_e32 v34, 0x3d372713, v32
	v_mul_f32_e32 v34, v34, v32
	v_fma_f32 v34, v34, v32, v32
	v_mul_f32_e32 v34, 0xc0135761, v34
	v_exp_f32_e32 v34, v34
	s_nop 0
	v_add_f32_e32 v34, 1.0, v34
	v_rcp_f32_e32 v34, v34
	s_nop 0
	v_mul_f32_e32 v32, v34, v32
	v_mul_f32_e32 v32, v33, v32
	v_cvt_pk_bf16_f32 v31, v31, v32
	global_store_dwordx2 v[60:61], v[30:31], off offset:96
	global_load_dwordx4 v[38:41], v[124:125], off
	global_load_dwordx4 v[34:37], v[126:127], off
	s_nop 0
	global_load_dwordx4 v[30:33], v[128:129], off
	global_load_dword v47, v[106:107], off offset:320
	ds_read_b128 v[42:45], v193
	ds_read_b128 v[60:63], v193 offset:64
	global_load_dwordx2 v[54:55], v[54:55], off
	s_waitcnt vmcnt(4) lgkmcnt(1)
	v_mfma_f32_16x16x32_bf16 v[42:45], v[42:45], v[38:41], 0
	s_waitcnt vmcnt(3) lgkmcnt(0)
	v_mfma_f32_16x16x32_bf16 v[42:45], v[60:63], v[34:37], v[42:45]
	ds_read_b128 v[60:63], v193 offset:128
	s_waitcnt vmcnt(2) lgkmcnt(0)
	v_mfma_f32_16x16x32_bf16 v[42:45], v[60:63], v[30:33], v[42:45]
	s_waitcnt vmcnt(0)
	v_lshlrev_b32_e32 v60, 16, v54
	v_mul_f32_e32 v61, 0x3d372713, v60
	v_mul_f32_e32 v61, v61, v60
	v_fma_f32 v61, v61, v60, v60
	v_mul_f32_e32 v61, 0xc0135761, v61
	v_exp_f32_e32 v61, v61
	s_nop 0
	v_add_f32_e32 v42, v47, v42
	v_and_b32_e32 v54, 0xffff0000, v54
	v_add_f32_e32 v43, v47, v43
	v_add_f32_e32 v61, 1.0, v61
	v_rcp_f32_e32 v61, v61
	v_add_f32_e32 v44, v47, v44
	v_add_f32_e32 v45, v47, v45
	v_mul_f32_e32 v60, v61, v60
	v_mul_f32_e32 v42, v42, v60
	v_mul_f32_e32 v60, 0x3d372713, v54
	v_mul_f32_e32 v60, v60, v54
	v_fma_f32 v60, v60, v54, v54
	v_mul_f32_e32 v60, 0xc0135761, v60
	v_exp_f32_e32 v60, v60
	s_nop 0
	v_add_f32_e32 v60, 1.0, v60
	v_rcp_f32_e32 v60, v60
	s_nop 0
	v_mul_f32_e32 v54, v60, v54
	v_mul_f32_e32 v43, v43, v54
	v_cvt_pk_bf16_f32 v42, v42, v43
	v_lshlrev_b32_e32 v43, 16, v55
	v_mul_f32_e32 v54, 0x3d372713, v43
	v_mul_f32_e32 v54, v54, v43
	v_fma_f32 v54, v54, v43, v43
	v_mul_f32_e32 v54, 0xc0135761, v54
	v_exp_f32_e32 v54, v54
	s_nop 0
	v_add_f32_e32 v54, 1.0, v54
	v_rcp_f32_e32 v54, v54
	s_nop 0
	v_mul_f32_e32 v43, v54, v43
	v_mul_f32_e32 v43, v44, v43
	v_and_b32_e32 v44, 0xffff0000, v55
	v_mul_f32_e32 v54, 0x3d372713, v44
	v_mul_f32_e32 v54, v54, v44
	v_fma_f32 v54, v54, v44, v44
	v_mul_f32_e32 v54, 0xc0135761, v54
	v_exp_f32_e32 v54, v54
	s_nop 0
	v_add_f32_e32 v54, 1.0, v54
	v_rcp_f32_e32 v54, v54
	s_nop 0
	v_mul_f32_e32 v44, v54, v44
	v_mul_f32_e32 v44, v45, v44
	v_cvt_pk_bf16_f32 v43, v43, v44
	global_load_dwordx2 v[52:53], v[52:53], off
	v_lshl_add_u64 v[54:55], v[138:139], 0, v[58:59]
	global_store_dwordx2 v[54:55], v[42:43], off
	ds_read_b128 v[42:45], v193 offset:4352
	ds_read_b128 v[58:61], v193 offset:4416
	s_waitcnt lgkmcnt(1)
	v_mfma_f32_16x16x32_bf16 v[42:45], v[42:45], v[38:41], 0
	s_waitcnt lgkmcnt(0)
	v_mfma_f32_16x16x32_bf16 v[42:45], v[58:61], v[34:37], v[42:45]
	ds_read_b128 v[58:61], v193 offset:4480
	s_waitcnt lgkmcnt(0)
	v_mfma_f32_16x16x32_bf16 v[42:45], v[58:61], v[30:33], v[42:45]
	s_waitcnt vmcnt(1)
	v_lshlrev_b32_e32 v58, 16, v52
	v_mul_f32_e32 v59, 0x3d372713, v58
	v_mul_f32_e32 v59, v59, v58
	v_fma_f32 v59, v59, v58, v58
	v_mul_f32_e32 v59, 0xc0135761, v59
	v_exp_f32_e32 v59, v59
	s_nop 0
	v_add_f32_e32 v42, v47, v42
	v_and_b32_e32 v52, 0xffff0000, v52
	v_add_f32_e32 v43, v47, v43
	v_add_f32_e32 v59, 1.0, v59
	v_rcp_f32_e32 v59, v59
	v_add_f32_e32 v44, v47, v44
	v_add_f32_e32 v45, v47, v45
	v_mul_f32_e32 v58, v59, v58
	v_mul_f32_e32 v42, v42, v58
	v_mul_f32_e32 v58, 0x3d372713, v52
	v_mul_f32_e32 v58, v58, v52
	v_fma_f32 v58, v58, v52, v52
	v_mul_f32_e32 v58, 0xc0135761, v58
	v_exp_f32_e32 v58, v58
	s_nop 0
	v_add_f32_e32 v58, 1.0, v58
	v_rcp_f32_e32 v58, v58
	s_nop 0
	v_mul_f32_e32 v52, v58, v52
	v_mul_f32_e32 v43, v43, v52
	v_cvt_pk_bf16_f32 v42, v42, v43
	v_lshlrev_b32_e32 v43, 16, v53
	v_mul_f32_e32 v52, 0x3d372713, v43
	v_mul_f32_e32 v52, v52, v43
	v_fma_f32 v52, v52, v43, v43
	v_mul_f32_e32 v52, 0xc0135761, v52
	v_exp_f32_e32 v52, v52
	s_nop 0
	v_add_f32_e32 v52, 1.0, v52
	v_rcp_f32_e32 v52, v52
	s_nop 0
	v_mul_f32_e32 v43, v52, v43
	v_mul_f32_e32 v43, v44, v43
	v_and_b32_e32 v44, 0xffff0000, v53
	v_mul_f32_e32 v52, 0x3d372713, v44
	v_mul_f32_e32 v52, v52, v44
	v_fma_f32 v52, v52, v44, v44
	v_mul_f32_e32 v52, 0xc0135761, v52
	v_exp_f32_e32 v52, v52
	s_nop 0
	v_add_f32_e32 v52, 1.0, v52
	v_rcp_f32_e32 v52, v52
	s_nop 0
	v_mul_f32_e32 v44, v52, v44
	v_mul_f32_e32 v44, v45, v44
	v_cvt_pk_bf16_f32 v43, v43, v44
	global_load_dwordx2 v[48:49], v[48:49], off
	ds_read_b128 v[58:61], v193 offset:8768
	global_store_dwordx2 v[54:55], v[42:43], off offset:32
	ds_read_b128 v[42:45], v193 offset:8704
	s_waitcnt lgkmcnt(0)
	v_mfma_f32_16x16x32_bf16 v[42:45], v[42:45], v[38:41], 0
	s_waitcnt vmcnt(1)
	v_lshlrev_b32_e32 v52, 16, v48
	v_mfma_f32_16x16x32_bf16 v[42:45], v[58:61], v[34:37], v[42:45]
	ds_read_b128 v[58:61], v193 offset:8832
	v_mul_f32_e32 v53, 0x3d372713, v52
	v_mul_f32_e32 v53, v53, v52
	v_fma_f32 v53, v53, v52, v52
	v_mul_f32_e32 v53, 0xc0135761, v53
	v_exp_f32_e32 v53, v53
	s_waitcnt lgkmcnt(0)
	v_mfma_f32_16x16x32_bf16 v[42:45], v[58:61], v[30:33], v[42:45]
	v_add_f32_e32 v53, 1.0, v53
	v_rcp_f32_e32 v53, v53
	v_and_b32_e32 v48, 0xffff0000, v48
	s_nop 4
	v_add_f32_e32 v42, v47, v42
	v_add_f32_e32 v43, v47, v43
	v_mul_f32_e32 v52, v53, v52
	v_mul_f32_e32 v42, v42, v52
	v_mul_f32_e32 v52, 0x3d372713, v48
	v_mul_f32_e32 v52, v52, v48
	v_fma_f32 v52, v52, v48, v48
	v_mul_f32_e32 v52, 0xc0135761, v52
	v_exp_f32_e32 v52, v52
	v_add_f32_e32 v44, v47, v44
	v_add_f32_e32 v45, v47, v45
	v_add_f32_e32 v52, 1.0, v52
	v_rcp_f32_e32 v52, v52
	s_nop 0
	v_mul_f32_e32 v48, v52, v48
	v_mul_f32_e32 v43, v43, v48
	v_cvt_pk_bf16_f32 v42, v42, v43
	v_lshlrev_b32_e32 v43, 16, v49
	v_mul_f32_e32 v48, 0x3d372713, v43
	v_mul_f32_e32 v48, v48, v43
	v_fma_f32 v48, v48, v43, v43
	v_mul_f32_e32 v48, 0xc0135761, v48
	v_exp_f32_e32 v48, v48
	s_nop 0
	v_add_f32_e32 v48, 1.0, v48
	v_rcp_f32_e32 v48, v48
	s_nop 0
	v_mul_f32_e32 v43, v48, v43
	v_mul_f32_e32 v43, v44, v43
	v_and_b32_e32 v44, 0xffff0000, v49
	v_mul_f32_e32 v48, 0x3d372713, v44
	v_mul_f32_e32 v48, v48, v44
	v_fma_f32 v48, v48, v44, v44
	v_mul_f32_e32 v48, 0xc0135761, v48
	v_exp_f32_e32 v48, v48
	s_nop 0
	v_add_f32_e32 v48, 1.0, v48
	v_rcp_f32_e32 v48, v48
	s_nop 0
	v_mul_f32_e32 v44, v48, v44
	v_mul_f32_e32 v44, v45, v44
	v_cvt_pk_bf16_f32 v43, v43, v44
	global_store_dwordx2 v[54:55], v[42:43], off offset:64
	ds_read_b128 v[42:45], v193 offset:13056
	s_waitcnt lgkmcnt(0)
	v_mfma_f32_16x16x32_bf16 v[38:41], v[42:45], v[38:41], 0
	ds_read_b128 v[42:45], v193 offset:13120
	s_waitcnt lgkmcnt(0)
	v_mfma_f32_16x16x32_bf16 v[34:37], v[42:45], v[34:37], v[38:41]
	s_nop 4
	ds_read_b128 v[38:41], v193 offset:13184
	s_waitcnt lgkmcnt(0)
	v_mfma_f32_16x16x32_bf16 v[30:33], v[38:41], v[30:33], v[34:37]
	s_nop 2
	v_lshl_add_u64 v[34:35], v[56:57], 0, v[50:51]
	global_load_dwordx2 v[34:35], v[34:35], off
	s_nop 2
	v_add_f32_e32 v30, v47, v30
	v_add_f32_e32 v31, v47, v31
	v_add_f32_e32 v32, v47, v32
	v_add_f32_e32 v33, v47, v33
	s_waitcnt vmcnt(0)
	v_lshlrev_b32_e32 v36, 16, v34
	v_mul_f32_e32 v37, 0x3d372713, v36
	v_mul_f32_e32 v37, v37, v36
	v_fma_f32 v37, v37, v36, v36
	v_mul_f32_e32 v37, 0xc0135761, v37
	v_exp_f32_e32 v37, v37
	v_and_b32_e32 v34, 0xffff0000, v34
	v_add_f32_e32 v37, 1.0, v37
	v_rcp_f32_e32 v37, v37
	s_nop 0
	v_mul_f32_e32 v36, v37, v36
	v_mul_f32_e32 v30, v30, v36
	v_mul_f32_e32 v36, 0x3d372713, v34
	v_mul_f32_e32 v36, v36, v34
	v_fma_f32 v36, v36, v34, v34
	v_mul_f32_e32 v36, 0xc0135761, v36
	v_exp_f32_e32 v36, v36
	s_nop 0
	v_add_f32_e32 v36, 1.0, v36
	v_rcp_f32_e32 v36, v36
	s_nop 0
	v_mul_f32_e32 v34, v36, v34
	v_mul_f32_e32 v31, v31, v34
	v_cvt_pk_bf16_f32 v30, v30, v31
	v_lshlrev_b32_e32 v31, 16, v35
	v_mul_f32_e32 v34, 0x3d372713, v31
	v_mul_f32_e32 v34, v34, v31
	v_fma_f32 v34, v34, v31, v31
	v_mul_f32_e32 v34, 0xc0135761, v34
	v_exp_f32_e32 v34, v34
	s_nop 0
	v_add_f32_e32 v34, 1.0, v34
	v_rcp_f32_e32 v34, v34
	s_nop 0
	v_mul_f32_e32 v31, v34, v31
	v_mul_f32_e32 v31, v32, v31
	v_and_b32_e32 v32, 0xffff0000, v35
	v_mul_f32_e32 v34, 0x3d372713, v32
	v_mul_f32_e32 v34, v34, v32
	v_fma_f32 v34, v34, v32, v32
	v_mul_f32_e32 v34, 0xc0135761, v34
	v_exp_f32_e32 v34, v34
	s_nop 0
	v_add_f32_e32 v34, 1.0, v34
	v_rcp_f32_e32 v34, v34
	s_nop 0
	v_mul_f32_e32 v32, v34, v32
	v_mul_f32_e32 v32, v33, v32
	v_cvt_pk_bf16_f32 v31, v31, v32
	global_store_dwordx2 v[54:55], v[30:31], off offset:96
.LBB0_382:
	v_lshl_or_b32 v198, s9, 12, v192
	v_lshl_add_u64 v[30:31], v[84:85], 0, v[198:199]
	global_load_dwordx4 v[42:45], v[30:31], off
	global_load_dwordx4 v[38:41], v[30:31], off offset:64
	global_load_dwordx4 v[34:37], v[30:31], off offset:128
	s_nop 0
	global_load_dwordx4 v[30:33], v[30:31], off offset:192
	ds_read_b128 v[52:55], v193
	ds_read_b128 v[56:59], v193 offset:64
	s_lshl_b32 s9, s9, 4
	v_or_b32_e32 v50, s9, v88
	v_ashrrev_i32_e32 v51, 31, v50
	v_lshl_add_u64 v[50:51], v[50:51], 2, s[2:3]
	v_or_b32_e32 v48, s9, v46
	global_load_dword v47, v[50:51], off
	v_mov_b64_e32 v[50:51], s[14:15]
	v_mad_i64_i32 v[50:51], s[12:13], v48, s16, v[50:51]
	v_lshl_add_u64 v[50:51], v[50:51], 0, s[18:19]
	v_ashrrev_i32_e32 v49, 31, v48
	v_lshlrev_b64 v[48:49], 10, v[48:49]
	v_lshl_add_u64 v[48:49], v[138:139], 0, v[48:49]
	s_mov_b32 s9, 7
	s_and_b64 vcc, exec, s[10:11]
	s_mov_b64 s[10:11], -1
	s_waitcnt vmcnt(4) lgkmcnt(1)
	v_mfma_f32_16x16x32_bf16 v[52:55], v[52:55], v[42:45], 0
	s_waitcnt vmcnt(3) lgkmcnt(0)
	v_mfma_f32_16x16x32_bf16 v[52:55], v[56:59], v[38:41], v[52:55]
	ds_read_b128 v[56:59], v193 offset:128
	s_waitcnt vmcnt(2) lgkmcnt(0)
	v_mfma_f32_16x16x32_bf16 v[52:55], v[56:59], v[34:37], v[52:55]
	ds_read_b128 v[56:59], v193 offset:192
	s_waitcnt vmcnt(1) lgkmcnt(0)
	v_mfma_f32_16x16x32_bf16 v[52:55], v[56:59], v[30:33], v[52:55]
	v_lshl_add_u64 v[56:57], v[90:91], 1, v[50:51]
	global_load_dwordx2 v[56:57], v[56:57], off
	v_lshl_add_u64 v[216:217], v[92:93], 1, v[50:51]
	global_load_dwordx2 v[216:217], v[216:217], off
	v_lshl_add_u64 v[218:219], v[94:95], 1, v[50:51]
	global_load_dwordx2 v[218:219], v[218:219], off
	v_lshl_add_u64 v[220:221], v[96:97], 1, v[50:51]
	global_load_dwordx2 v[220:221], v[220:221], off
	s_waitcnt vmcnt(1)
	s_nop 4
	v_add_f32_e32 v52, v47, v52
	v_add_f32_e32 v53, v47, v53
	v_add_f32_e32 v54, v47, v54
	v_add_f32_e32 v55, v47, v55
	s_waitcnt vmcnt(0)
	v_lshlrev_b32_e32 v58, 16, v56
	v_mul_f32_e32 v59, 0x3d372713, v58
	v_mul_f32_e32 v59, v59, v58
	v_fma_f32 v59, v59, v58, v58
	v_mul_f32_e32 v59, 0xc0135761, v59
	v_exp_f32_e32 v59, v59
	v_and_b32_e32 v56, 0xffff0000, v56
	v_add_f32_e32 v59, 1.0, v59
	v_rcp_f32_e32 v59, v59
	s_nop 0
	v_mul_f32_e32 v58, v59, v58
	v_mul_f32_e32 v52, v52, v58
	v_mul_f32_e32 v58, 0x3d372713, v56
	v_mul_f32_e32 v58, v58, v56
	v_fma_f32 v58, v58, v56, v56
	v_mul_f32_e32 v58, 0xc0135761, v58
	v_exp_f32_e32 v58, v58
	s_nop 0
	v_add_f32_e32 v58, 1.0, v58
	v_rcp_f32_e32 v58, v58
	s_nop 0
	v_mul_f32_e32 v56, v58, v56
	v_mul_f32_e32 v53, v53, v56
	v_cvt_pk_bf16_f32 v52, v52, v53
	v_lshlrev_b32_e32 v53, 16, v57
	v_mul_f32_e32 v56, 0x3d372713, v53
	v_mul_f32_e32 v56, v56, v53
	v_fma_f32 v56, v56, v53, v53
	v_mul_f32_e32 v56, 0xc0135761, v56
	v_exp_f32_e32 v56, v56
	s_nop 0
	v_add_f32_e32 v56, 1.0, v56
	v_rcp_f32_e32 v56, v56
	s_nop 0
	v_mul_f32_e32 v53, v56, v53
	v_mul_f32_e32 v53, v54, v53
	v_and_b32_e32 v54, 0xffff0000, v57
	v_mul_f32_e32 v56, 0x3d372713, v54
	v_mul_f32_e32 v56, v56, v54
	v_fma_f32 v56, v56, v54, v54
	v_mul_f32_e32 v56, 0xc0135761, v56
	v_exp_f32_e32 v56, v56
	s_nop 0
	v_add_f32_e32 v56, 1.0, v56
	v_rcp_f32_e32 v56, v56
	s_nop 0
	v_mul_f32_e32 v54, v56, v54
	v_mul_f32_e32 v54, v55, v54
	v_cvt_pk_bf16_f32 v53, v53, v54
	global_store_dwordx2 v[48:49], v[52:53], off
	ds_read_b128 v[52:55], v193 offset:4352
	ds_read_b128 v[56:59], v193 offset:4416
	s_waitcnt lgkmcnt(1)
	v_mfma_f32_16x16x32_bf16 v[52:55], v[52:55], v[42:45], 0
	s_waitcnt lgkmcnt(0)
	v_mfma_f32_16x16x32_bf16 v[52:55], v[56:59], v[38:41], v[52:55]
	ds_read_b128 v[56:59], v193 offset:4480
	s_waitcnt lgkmcnt(0)
	v_mfma_f32_16x16x32_bf16 v[52:55], v[56:59], v[34:37], v[52:55]
	ds_read_b128 v[56:59], v193 offset:4544
	s_waitcnt lgkmcnt(0)
	v_mfma_f32_16x16x32_bf16 v[52:55], v[56:59], v[30:33], v[52:55]
	v_lshl_add_u64 v[56:57], v[92:93], 1, v[50:51]
	s_nop 5
	v_add_f32_e32 v52, v47, v52
	v_add_f32_e32 v53, v47, v53
	v_add_f32_e32 v54, v47, v54
	v_add_f32_e32 v55, v47, v55
	s_waitcnt vmcnt(2)
	v_mov_b64_e32 v[56:57], v[216:217]
	v_lshlrev_b32_e32 v58, 16, v56
	v_mul_f32_e32 v59, 0x3d372713, v58
	v_mul_f32_e32 v59, v59, v58
	v_fma_f32 v59, v59, v58, v58
	v_mul_f32_e32 v59, 0xc0135761, v59
	v_exp_f32_e32 v59, v59
	v_and_b32_e32 v56, 0xffff0000, v56
	v_add_f32_e32 v59, 1.0, v59
	v_rcp_f32_e32 v59, v59
	s_nop 0
	v_mul_f32_e32 v58, v59, v58
	v_mul_f32_e32 v52, v52, v58
	v_mul_f32_e32 v58, 0x3d372713, v56
	v_mul_f32_e32 v58, v58, v56
	v_fma_f32 v58, v58, v56, v56
	v_mul_f32_e32 v58, 0xc0135761, v58
	v_exp_f32_e32 v58, v58
	s_nop 0
	v_add_f32_e32 v58, 1.0, v58
	v_rcp_f32_e32 v58, v58
	s_nop 0
	v_mul_f32_e32 v56, v58, v56
	v_mul_f32_e32 v53, v53, v56
	v_cvt_pk_bf16_f32 v52, v52, v53
	v_lshlrev_b32_e32 v53, 16, v57
	v_mul_f32_e32 v56, 0x3d372713, v53
	v_mul_f32_e32 v56, v56, v53
	v_fma_f32 v56, v56, v53, v53
	v_mul_f32_e32 v56, 0xc0135761, v56
	v_exp_f32_e32 v56, v56
	s_nop 0
	v_add_f32_e32 v56, 1.0, v56
	v_rcp_f32_e32 v56, v56
	s_nop 0
	v_mul_f32_e32 v53, v56, v53
	v_mul_f32_e32 v53, v54, v53
	v_and_b32_e32 v54, 0xffff0000, v57
	v_mul_f32_e32 v56, 0x3d372713, v54
	v_mul_f32_e32 v56, v56, v54
	v_fma_f32 v56, v56, v54, v54
	v_mul_f32_e32 v56, 0xc0135761, v56
	v_exp_f32_e32 v56, v56
	s_nop 0
	v_add_f32_e32 v56, 1.0, v56
	v_rcp_f32_e32 v56, v56
	s_nop 0
	v_mul_f32_e32 v54, v56, v54
	v_mul_f32_e32 v54, v55, v54
	v_cvt_pk_bf16_f32 v53, v53, v54
	global_store_dwordx2 v[48:49], v[52:53], off offset:32
	ds_read_b128 v[52:55], v193 offset:8704
	ds_read_b128 v[56:59], v193 offset:8768
	s_waitcnt lgkmcnt(1)
	v_mfma_f32_16x16x32_bf16 v[52:55], v[52:55], v[42:45], 0
	s_waitcnt lgkmcnt(0)
	v_mfma_f32_16x16x32_bf16 v[52:55], v[56:59], v[38:41], v[52:55]
	ds_read_b128 v[56:59], v193 offset:8832
	s_waitcnt lgkmcnt(0)
	v_mfma_f32_16x16x32_bf16 v[52:55], v[56:59], v[34:37], v[52:55]
	ds_read_b128 v[56:59], v193 offset:8896
	s_waitcnt lgkmcnt(0)
	v_mfma_f32_16x16x32_bf16 v[52:55], v[56:59], v[30:33], v[52:55]
	v_lshl_add_u64 v[56:57], v[94:95], 1, v[50:51]
	s_nop 5
	v_add_f32_e32 v52, v47, v52
	v_add_f32_e32 v53, v47, v53
	v_add_f32_e32 v54, v47, v54
	v_add_f32_e32 v55, v47, v55
	s_waitcnt vmcnt(2)
	v_mov_b64_e32 v[56:57], v[218:219]
	v_lshlrev_b32_e32 v58, 16, v56
	v_mul_f32_e32 v59, 0x3d372713, v58
	v_mul_f32_e32 v59, v59, v58
	v_fma_f32 v59, v59, v58, v58
	v_mul_f32_e32 v59, 0xc0135761, v59
	v_exp_f32_e32 v59, v59
	v_and_b32_e32 v56, 0xffff0000, v56
	v_add_f32_e32 v59, 1.0, v59
	v_rcp_f32_e32 v59, v59
	s_nop 0
	v_mul_f32_e32 v58, v59, v58
	v_mul_f32_e32 v52, v52, v58
	v_mul_f32_e32 v58, 0x3d372713, v56
	v_mul_f32_e32 v58, v58, v56
	v_fma_f32 v58, v58, v56, v56
	v_mul_f32_e32 v58, 0xc0135761, v58
	v_exp_f32_e32 v58, v58
	s_nop 0
	v_add_f32_e32 v58, 1.0, v58
	v_rcp_f32_e32 v58, v58
	s_nop 0
	v_mul_f32_e32 v56, v58, v56
	v_mul_f32_e32 v53, v53, v56
	v_cvt_pk_bf16_f32 v52, v52, v53
	v_lshlrev_b32_e32 v53, 16, v57
	v_mul_f32_e32 v56, 0x3d372713, v53
	v_mul_f32_e32 v56, v56, v53
	v_fma_f32 v56, v56, v53, v53
	v_mul_f32_e32 v56, 0xc0135761, v56
	v_exp_f32_e32 v56, v56
	s_nop 0
	v_add_f32_e32 v56, 1.0, v56
	v_rcp_f32_e32 v56, v56
	s_nop 0
	v_mul_f32_e32 v53, v56, v53
	v_mul_f32_e32 v53, v54, v53
	v_and_b32_e32 v54, 0xffff0000, v57
	v_mul_f32_e32 v56, 0x3d372713, v54
	v_mul_f32_e32 v56, v56, v54
	v_fma_f32 v56, v56, v54, v54
	v_mul_f32_e32 v56, 0xc0135761, v56
	v_exp_f32_e32 v56, v56
	s_nop 0
	v_add_f32_e32 v56, 1.0, v56
	v_rcp_f32_e32 v56, v56
	s_nop 0
	v_mul_f32_e32 v54, v56, v54
	v_mul_f32_e32 v54, v55, v54
	v_cvt_pk_bf16_f32 v53, v53, v54
	global_store_dwordx2 v[48:49], v[52:53], off offset:64
	ds_read_b128 v[52:55], v193 offset:13056
	s_waitcnt lgkmcnt(0)
	v_mfma_f32_16x16x32_bf16 v[42:45], v[52:55], v[42:45], 0
	ds_read_b128 v[52:55], v193 offset:13120
	s_waitcnt lgkmcnt(0)
	v_mfma_f32_16x16x32_bf16 v[38:41], v[52:55], v[38:41], v[42:45]
	s_nop 4
	ds_read_b128 v[42:45], v193 offset:13184
	s_waitcnt lgkmcnt(0)
	v_mfma_f32_16x16x32_bf16 v[34:37], v[42:45], v[34:37], v[38:41]
	s_nop 2
	ds_read_b128 v[38:41], v193 offset:13248
	s_waitcnt lgkmcnt(0)
	v_mfma_f32_16x16x32_bf16 v[30:33], v[38:41], v[30:33], v[34:37]
	s_nop 2
	v_lshl_add_u64 v[34:35], v[96:97], 1, v[50:51]
	s_nop 2
	v_add_f32_e32 v30, v47, v30
	v_add_f32_e32 v31, v47, v31
	v_add_f32_e32 v32, v47, v32
	v_add_f32_e32 v33, v47, v33
	s_waitcnt vmcnt(3)
	v_mov_b64_e32 v[34:35], v[220:221]
	v_lshlrev_b32_e32 v36, 16, v34
	v_mul_f32_e32 v37, 0x3d372713, v36
	v_mul_f32_e32 v37, v37, v36
	v_fma_f32 v37, v37, v36, v36
	v_mul_f32_e32 v37, 0xc0135761, v37
	v_exp_f32_e32 v37, v37
	v_and_b32_e32 v34, 0xffff0000, v34
	v_add_f32_e32 v37, 1.0, v37
	v_rcp_f32_e32 v37, v37
	s_nop 0
	v_mul_f32_e32 v36, v37, v36
	v_mul_f32_e32 v30, v30, v36
	v_mul_f32_e32 v36, 0x3d372713, v34
	v_mul_f32_e32 v36, v36, v34
	v_fma_f32 v36, v36, v34, v34
	v_mul_f32_e32 v36, 0xc0135761, v36
	v_exp_f32_e32 v36, v36
	s_nop 0
	v_add_f32_e32 v36, 1.0, v36
	v_rcp_f32_e32 v36, v36
	s_nop 0
	v_mul_f32_e32 v34, v36, v34
	v_mul_f32_e32 v31, v31, v34
	v_cvt_pk_bf16_f32 v30, v30, v31
	v_lshlrev_b32_e32 v31, 16, v35
	v_mul_f32_e32 v34, 0x3d372713, v31
	v_mul_f32_e32 v34, v34, v31
	v_fma_f32 v34, v34, v31, v31
	v_mul_f32_e32 v34, 0xc0135761, v34
	v_exp_f32_e32 v34, v34
	s_nop 0
	v_add_f32_e32 v34, 1.0, v34
	v_rcp_f32_e32 v34, v34
	s_nop 0
	v_mul_f32_e32 v31, v34, v31
	v_mul_f32_e32 v31, v32, v31
	v_and_b32_e32 v32, 0xffff0000, v35
	v_mul_f32_e32 v34, 0x3d372713, v32
	v_mul_f32_e32 v34, v34, v32
	v_fma_f32 v34, v34, v32, v32
	v_mul_f32_e32 v34, 0xc0135761, v34
	v_exp_f32_e32 v34, v34
	s_nop 0
	v_add_f32_e32 v34, 1.0, v34
	v_rcp_f32_e32 v34, v34
	s_nop 0
	v_mul_f32_e32 v32, v34, v32
	v_mul_f32_e32 v32, v33, v32
	v_cvt_pk_bf16_f32 v31, v31, v32
	global_store_dwordx2 v[48:49], v[30:31], off offset:96
	s_cbranch_vccz .LBB0_382
	s_add_i32 s21, s21, s20
	s_add_i32 s23, s23, s24
	s_add_i32 s8, s8, s24
	s_cmpk_gt_i32 s21, 0xff
	s_barrier
	s_cbranch_scc0 .LBB0_345
	s_movk_i32 s40, 0x3fff

.LBB0_672:
	v_readlane_b32 s0, v254, 17
	s_waitcnt lgkmcnt(0)
	s_barrier
	v_mov_b32_e32 v10, s0
	ds_read_b32 v10, v10
	v_readlane_b32 s0, v254, 29
	s_waitcnt lgkmcnt(0)
	v_readfirstlane_b32 s9, v10
	v_cmp_ge_i32_e32 vcc, s0, v10
	s_cbranch_vccnz .LBB0_708
	v_mov_b32_e32 v10, s24
	ds_read_u16 v42, v10
	s_lshl_b64 s[10:11], s[10:11], 1
	v_readlane_b32 s0, v253, 0
	s_add_u32 s0, s0, s10
	v_readlane_b32 s1, v253, 1
	s_addc_u32 s1, s1, s11
	v_readlane_b32 s12, v252, 60
	v_readlane_b32 s13, v252, 61
	s_add_u32 s10, s12, s10
	s_waitcnt lgkmcnt(0)
	v_readfirstlane_b32 s12, v42
	s_addc_u32 s11, s13, s11
	s_mov_b32 s98, s12
	s_and_b32 s12, s12, 63
	s_lshl_b32 s13, s12, 13
	v_mov_b32_e32 v135, v199
	v_lshl_or_b32 v198, v181, 7, s13
	v_lshl_add_u64 v[98:99], s[0:1], 0, v[134:135]
	v_mov_b32_e32 v137, v199
	v_lshl_add_u64 v[10:11], s[10:11], 0, v[198:199]
	s_add_u32 s0, s0, s13
	v_lshl_add_u64 v[14:15], v[10:11], 0, v[136:137]
	s_addc_u32 s1, s1, 0
	global_load_dwordx4 v[18:21], v[14:15], off offset:3072
	global_load_dwordx4 v[22:25], v[14:15], off offset:2048
	global_load_dwordx4 v[10:13], v[14:15], off offset:1024
	s_nop 0
	global_load_dwordx4 v[14:17], v[14:15], off
	s_nop 0
	global_load_dwordx4 v[26:29], v134, s[0:1] offset:3072
	global_load_dwordx4 v[30:33], v134, s[0:1] offset:2048
	global_load_dwordx4 v[34:37], v134, s[0:1] offset:1024
	global_load_dwordx4 v[38:41], v134, s[0:1]
	s_lshl_b32 s0, s12, 2
	s_add_i32 s0, s0, 0
	s_add_i32 s0, s0, 0x12800
	v_mov_b32_e32 v43, s0
	ds_read_b32 v43, v43
	v_lshrrev_b32_e32 v42, 6, v42
	s_lshl_b32 s0, s12, 7
	v_and_or_b32 v42, v42, 60, v230
	s_add_i32 s0, s0, 0
	s_waitcnt lgkmcnt(0)
	v_cmp_lt_i32_e32 vcc, v42, v43
	v_lshl_add_u32 v42, v42, 1, s0
	v_add_u32_e32 v42, 0x12c00, v42
	ds_read_u16 v42, v42
	s_lshl_b32 s92, s35, 1
	v_mov_b32_e32 v139, v199
	v_lshl_add_u64 v[100:101], s[10:11], 0, v[136:137]
	v_lshl_add_u64 v[102:103], s[4:5], 0, v[138:139]
	s_waitcnt lgkmcnt(0)
	v_and_b32_e32 v42, 63, v42
	v_and_b32_e32 v42, 0xffff, v42
	v_cndmask_b32_e32 v42, 0, v42, vcc
	v_or_b32_e32 v42, s31, v42
	v_mul_u32_u24_e32 v42, 0x1400, v42
	v_lshlrev_b32_e32 v198, 1, v42
	v_lshl_add_u64 v[42:43], s[6:7], 0, v[198:199]
	v_lshl_add_u64 v[42:43], v[42:43], 0, s[92:93]
	v_lshl_add_u64 v[46:47], v[42:43], 0, v[138:139]
	global_load_dwordx4 v[42:45], v[46:47], off offset:3328
	v_readlane_b32 s14, v254, 29
	s_waitcnt vmcnt(0)
	v_cndmask_b32_e32 v69, 0, v45, vcc
	v_cndmask_b32_e32 v68, 0, v44, vcc
	v_cndmask_b32_e32 v67, 0, v43, vcc
	v_cndmask_b32_e32 v66, 0, v42, vcc
	global_load_dwordx4 v[42:45], v[46:47], off offset:3072
	s_waitcnt vmcnt(0)
	v_cndmask_b32_e32 v65, 0, v45, vcc
	v_cndmask_b32_e32 v64, 0, v44, vcc
	v_cndmask_b32_e32 v63, 0, v43, vcc
	v_cndmask_b32_e32 v62, 0, v42, vcc
	s_branch .LBB0_675

.LBB0_675:
	v_mfma_f32_16x16x32_bf16 v[38:41], v[38:41], v[62:65], 0
	s_mov_b32 s0, s98
	s_and_b32 s4, s0, 0xff
	s_and_b32 s1, s0, 0xffff
	s_lshl_b32 s0, s4, 2
	s_add_i32 s0, s0, 0
	s_add_i32 s0, s0, 0x12800
	v_mov_b32_e32 v42, s0
	s_bfe_u32 s0, s1, 0x80008
	s_lshl_b32 s1, s4, 7
	s_lshl_b32 s16, s0, 2
	s_lshl_b32 s0, s4, 6
	s_add_i32 s17, s1, 0
	v_or_b32_e32 v71, s16, v230
	s_add_i32 s17, s17, 0x12c00
	s_or_b32 s0, s0, 32
	ds_read_b32 v70, v42
	v_lshl_add_u32 v42, v71, 1, s17
	s_lshl_b32 s92, s0, 7
	ds_read_u8 v72, v42
	v_lshl_add_u64 v[42:43], v[98:99], 0, s[92:93]
	global_load_dwordx4 v[94:97], v[42:43], off
	global_load_dwordx4 v[90:93], v[42:43], off offset:1024
	global_load_dwordx4 v[58:61], v[42:43], off offset:2048
	global_load_dwordx4 v[86:89], v[42:43], off offset:3072
	v_or_b32_e32 v42, s0, v181
	v_lshlrev_b32_e32 v198, 7, v42
	v_lshl_add_u64 v[54:55], v[100:101], 0, v[198:199]
	global_load_dwordx4 v[42:45], v[54:55], off
	global_load_dwordx4 v[46:49], v[54:55], off offset:1024
	global_load_dwordx4 v[50:53], v[54:55], off offset:2048
	s_nop 0
	global_load_dwordx4 v[54:57], v[54:55], off offset:3072
	v_mfma_f32_16x16x32_bf16 v[30:33], v[30:33], v[62:65], 0
	s_waitcnt lgkmcnt(1)
	v_readfirstlane_b32 s18, v70
	s_sub_i32 s35, s34, s4
	s_lshl_b32 s4, s35, 6
	v_cmp_gt_i32_e64 s[0:1], s18, v71
	v_mfma_f32_16x16x32_bf16 v[34:37], v[34:37], v[66:69], v[38:41]
	s_cmp_lt_i32 s35, 17
	s_waitcnt lgkmcnt(0)
	v_cndmask_b32_e64 v106, -1, v72, s[0:1]
	s_cselect_b64 s[12:13], -1, 0
	v_mfma_f32_16x16x32_bf16 v[26:29], v[26:29], v[66:69], v[30:33]
	s_and_b64 vcc, exec, s[12:13]
	s_nop 1
	v_max_i32_e32 v30, 0, v106
	v_sub_u32_e32 v31, s4, v231
	v_add_u32_e32 v107, v30, v31
	s_mov_b64 s[4:5], -1
	s_cbranch_vccz .LBB0_681
	s_add_i32 s4, s35, -1
	s_cmp_lt_u32 s4, 14
	s_mov_b64 s[4:5], -1
	s_cbranch_scc1 .LBB0_678
	v_add_u32_e32 v32, -1, v107
	v_add_u32_e32 v38, -2, v107
	v_med3_i32 v31, v107, 16, v239
	v_med3_i32 v33, v32, 0, v236
	v_med3_i32 v32, v32, 16, v239
	v_med3_i32 v39, v38, 0, v236
	v_med3_i32 v38, v38, 16, v239
	v_add_u32_e32 v40, -3, v107
	v_med3_i32 v30, v107, 0, v236
	v_lshlrev_b32_e32 v31, 2, v31
	s_movk_i32 s4, 0xffc0
	v_lshlrev_b32_e32 v32, 2, v32
	v_lshlrev_b32_e32 v38, 2, v38
	v_med3_i32 v41, v40, 0, v236
	v_med3_i32 v40, v40, 16, v239
	v_lshl_add_u32 v30, v30, 2, v210
	v_add3_u32 v31, v210, v31, s4
	v_lshl_add_u32 v33, v33, 2, v210
	v_add3_u32 v32, v210, v32, s4
	v_lshl_add_u32 v39, v39, 2, v210
	v_add3_u32 v38, v210, v38, s4
	v_lshlrev_b32_e32 v40, 2, v40
	v_lshl_add_u32 v41, v41, 2, v210
	v_add3_u32 v40, v210, v40, s4
	ds_read_b32 v30, v30
	ds_read_b32 v31, v31
	ds_read_b32 v33, v33
	ds_read_b32 v32, v32
	ds_read_b32 v39, v39
	ds_read_b32 v38, v38
	ds_read_b32 v71, v41
	ds_read_b32 v72, v40
	s_waitcnt lgkmcnt(7)
	v_add_f32_e32 v30, v34, v30
	v_exp_f32_e32 v30, v30
	s_waitcnt lgkmcnt(6)
	v_add_f32_e32 v31, v26, v31
	v_exp_f32_e32 v31, v31
	v_cmp_lt_i32_e32 vcc, -1, v107
	s_and_b64 vcc, s[0:1], vcc
	s_waitcnt lgkmcnt(4)
	v_add_f32_e32 v32, v27, v32
	v_cndmask_b32_e32 v40, 0, v30, vcc
	v_cmp_lt_i32_e32 vcc, 15, v107
	s_and_b64 vcc, s[0:1], vcc
	v_exp_f32_e32 v32, v32
	v_cndmask_b32_e32 v41, 0, v31, vcc
	v_add_f32_e32 v30, v40, v41
	v_add_f32_e32 v31, 0, v30
	v_add_f32_e32 v30, v35, v33
	v_exp_f32_e32 v30, v30
	v_cmp_lt_i32_e32 vcc, 0, v107
	s_and_b64 vcc, s[0:1], vcc
	s_waitcnt lgkmcnt(2)
	v_add_f32_e32 v33, v28, v38
	v_cndmask_b32_e32 v30, 0, v30, vcc
	v_cmp_lt_i32_e32 vcc, 16, v107
	s_and_b64 vcc, s[0:1], vcc
	v_exp_f32_e32 v33, v33
	v_cndmask_b32_e32 v198, 0, v32, vcc
	v_add_f32_e32 v32, v30, v198
	v_add_f32_e32 v32, v31, v32
	v_add_f32_e32 v31, v36, v39
	v_exp_f32_e32 v31, v31
	v_cmp_lt_i32_e32 vcc, 1, v107
	s_and_b64 vcc, s[0:1], vcc
	s_waitcnt lgkmcnt(0)
	v_add_f32_e32 v38, v29, v72
	v_cndmask_b32_e32 v31, 0, v31, vcc
	v_cmp_lt_i32_e32 vcc, 17, v107
	s_and_b64 vcc, s[0:1], vcc
	v_exp_f32_e32 v38, v38
	v_cndmask_b32_e32 v70, 0, v33, vcc
	v_add_f32_e32 v33, v31, v70
	v_add_f32_e32 v33, v32, v33
	v_add_f32_e32 v32, v37, v71
	v_exp_f32_e32 v32, v32
	v_cmp_lt_i32_e32 vcc, 2, v107
	s_and_b64 vcc, s[0:1], vcc
	s_mov_b64 s[4:5], 0
	v_cndmask_b32_e32 v32, 0, v32, vcc
	v_cmp_lt_i32_e32 vcc, 18, v107
	s_and_b64 vcc, s[0:1], vcc
	s_nop 0
	v_cndmask_b32_e32 v38, 0, v38, vcc
	v_add_f32_e32 v39, v32, v38
	v_add_f32_e32 v105, v33, v39

.LBB0_683:
	s_add_i32 s19, s14, 8
	s_cmp_ge_i32 s19, s9
	s_cselect_b64 s[10:11], -1, 0
	s_cmp_lt_i32 s19, s9
	s_cselect_b32 s4, s19, s14
	ds_write_b128 v208, v[14:17]
	ds_write_b128 v208, v[10:13] offset:1152
	ds_write_b128 v208, v[22:25] offset:2304
	ds_write_b128 v208, v[18:21] offset:3456
	s_lshl_b32 s4, s4, 1
	v_cvt_pk_bf16_f32 v10, v40, v30
	v_cvt_pk_bf16_f32 v11, v31, v32
	v_cvt_pk_bf16_f32 v12, v41, v198
	v_cvt_pk_bf16_f32 v13, v70, v38
	ds_read_b64_tr_b16 v[16:17], v209 offset:2304
	ds_read_b64_tr_b16 v[14:15], v209
	ds_read_b64_tr_b16 v[18:19], v209 offset:32
	ds_read_b64_tr_b16 v[22:23], v209 offset:64
	ds_read_b64_tr_b16 v[26:27], v209 offset:96
	ds_read_b64_tr_b16 v[20:21], v209 offset:2336
	ds_read_b64_tr_b16 v[24:25], v209 offset:2368
	ds_read_b64_tr_b16 v[28:29], v209 offset:2400
	s_add_i32 s4, s4, 0
	s_add_i32 s4, s4, 0x12900
	s_waitcnt lgkmcnt(6)
	v_mfma_f32_16x16x32_bf16 v[70:73], v[10:13], v[14:17], 0
	v_mov_b32_e32 v14, s4
	s_mov_b64 s[14:15], -1
	s_waitcnt lgkmcnt(2)
	v_mfma_f32_16x16x32_bf16 v[74:77], v[10:13], v[18:21], 0
	ds_read_u16 v20, v14
	s_and_b64 vcc, exec, s[12:13]
	s_waitcnt lgkmcnt(0)
	v_readfirstlane_b32 s4, v20
	s_mov_b32 s98, s4
	s_and_b32 s4, s4, 63
	v_lshrrev_b32_e32 v20, 6, v20
	s_lshl_b32 s5, s4, 7
	s_lshl_b32 s92, s4, 13
	v_and_or_b32 v104, v20, 60, v230
	s_add_i32 s5, s5, 0
	s_lshl_b32 s4, s4, 2
	v_lshl_or_b32 v198, v181, 7, s92
	v_lshl_add_u32 v20, v104, 1, s5
	s_add_i32 s4, s4, 0
	v_mfma_f32_16x16x32_bf16 v[78:81], v[10:13], v[22:25], 0
	v_lshl_add_u64 v[18:19], v[100:101], 0, v[198:199]
	v_add_u32_e32 v20, 0x12c00, v20
	s_add_i32 s4, s4, 0x12800
	v_mfma_f32_16x16x32_bf16 v[82:85], v[10:13], v[26:29], 0
	v_lshl_add_u64 v[10:11], v[98:99], 0, s[92:93]
	global_load_dwordx4 v[38:41], v[10:11], off
	global_load_dwordx4 v[34:37], v[10:11], off offset:1024
	global_load_dwordx4 v[30:33], v[10:11], off offset:2048
	global_load_dwordx4 v[26:29], v[10:11], off offset:3072
	global_load_dwordx4 v[14:17], v[18:19], off
	s_nop 0
	global_load_dwordx4 v[10:13], v[18:19], off offset:1024
	ds_read_u16 v108, v20
	v_mov_b32_e32 v20, s4
	ds_read_b32 v109, v20
	s_waitcnt vmcnt(13)
	v_mfma_f32_16x16x32_bf16 v[94:97], v[94:97], v[62:65], 0
	global_load_dwordx4 v[22:25], v[18:19], off offset:2048
	s_nop 0
	global_load_dwordx4 v[18:21], v[18:19], off offset:3072
	s_waitcnt lgkmcnt(1)
	v_and_b32_e32 v108, 63, v108
	v_and_b32_e32 v108, 0xffff, v108
	s_waitcnt lgkmcnt(0)
	v_cmp_lt_i32_e64 s[4:5], v104, v109
	s_waitcnt vmcnt(14)
	v_mfma_f32_16x16x32_bf16 v[90:93], v[90:93], v[66:69], v[94:97]
	v_cndmask_b32_e64 v104, 0, v108, s[4:5]
	v_or_b32_e32 v104, s31, v104
	s_nop 0
	v_mul_u32_u24_e32 v94, 0x1400, v104
	v_lshlrev_b32_e32 v198, 1, v94
	v_lshl_add_u64 v[108:109], v[102:103], 0, v[198:199]
	s_waitcnt vmcnt(13)
	v_mfma_f32_16x16x32_bf16 v[94:97], v[58:61], v[62:65], 0
	global_load_dwordx4 v[62:65], v[108:109], off offset:3072
	global_load_dwordx4 v[58:61], v[108:109], off offset:3328
	s_waitcnt vmcnt(14)
	v_mfma_f32_16x16x32_bf16 v[66:69], v[86:89], v[66:69], v[94:97]
	s_cbranch_vccz .LBB0_689
	s_add_i32 s35, s35, -1
	v_subrev_u32_e32 v87, 32, v107
	s_cmp_lt_u32 s35, 14
	s_mov_b64 s[12:13], -1
	s_cbranch_scc1 .LBB0_686
	v_med3_i32 v86, v87, 0, v236
	v_lshl_add_u32 v86, v86, 2, v210
	v_med3_i32 v88, v87, 16, v239
	ds_read_b32 v86, v86
	v_lshlrev_b32_e32 v88, 2, v88
	s_movk_i32 s12, 0xffc0
	v_add3_u32 v88, v210, v88, s12
	ds_read_b32 v88, v88
	s_waitcnt lgkmcnt(1)
	v_add_f32_e32 v86, v90, v86
	v_exp_f32_e32 v86, v86
	v_cmp_lt_i32_e32 vcc, 31, v107
	s_and_b64 vcc, s[0:1], vcc
	s_waitcnt lgkmcnt(0)
	v_add_f32_e32 v88, v66, v88
	v_exp_f32_e32 v88, v88
	v_cndmask_b32_e32 v96, 0, v86, vcc
	v_cmp_lt_i32_e32 vcc, 47, v107
	s_and_b64 vcc, s[0:1], vcc
	s_nop 0
	v_cndmask_b32_e32 v97, 0, v88, vcc
	v_add_f32_e32 v86, v96, v97
	v_add_f32_e32 v88, v105, v86
	v_subrev_u32_e32 v86, 33, v107
	v_med3_i32 v89, v86, 0, v236
	v_lshl_add_u32 v89, v89, 2, v210
	v_med3_i32 v86, v86, 16, v239
	ds_read_b32 v89, v89
	v_lshlrev_b32_e32 v86, 2, v86
	v_add3_u32 v86, v210, v86, s12
	ds_read_b32 v86, v86
	v_cmp_lt_i32_e32 vcc, 32, v107
	s_waitcnt lgkmcnt(1)
	v_add_f32_e32 v89, v91, v89
	v_exp_f32_e32 v89, v89
	s_and_b64 vcc, s[0:1], vcc
	s_waitcnt lgkmcnt(0)
	v_add_f32_e32 v86, v67, v86
	v_exp_f32_e32 v86, v86
	v_cndmask_b32_e32 v104, 0, v89, vcc
	v_cmp_lt_i32_e32 vcc, 48, v107
	s_and_b64 vcc, s[0:1], vcc
	s_nop 0
	v_cndmask_b32_e32 v86, 0, v86, vcc
	v_add_f32_e32 v89, v104, v86
	v_add_f32_e32 v88, v88, v89
	v_subrev_u32_e32 v89, 34, v107
	v_med3_i32 v94, v89, 0, v236
	v_lshl_add_u32 v94, v94, 2, v210
	v_med3_i32 v89, v89, 16, v239
	ds_read_b32 v94, v94
	v_lshlrev_b32_e32 v89, 2, v89
	v_add3_u32 v89, v210, v89, s12
	ds_read_b32 v89, v89
	v_cmp_lt_i32_e32 vcc, 33, v107
	s_waitcnt lgkmcnt(1)
	v_add_f32_e32 v94, v92, v94
	v_exp_f32_e32 v94, v94
	s_and_b64 vcc, s[0:1], vcc
	s_waitcnt lgkmcnt(0)
	v_add_f32_e32 v89, v68, v89
	v_exp_f32_e32 v89, v89
	v_cndmask_b32_e32 v108, 0, v94, vcc
	v_cmp_lt_i32_e32 vcc, 49, v107
	s_and_b64 vcc, s[0:1], vcc
	s_nop 0
	v_cndmask_b32_e32 v109, 0, v89, vcc
	v_add_f32_e32 v89, v108, v109
	v_add_f32_e32 v89, v88, v89
	v_subrev_u32_e32 v88, 35, v107
	v_med3_i32 v94, v88, 0, v236
	v_lshl_add_u32 v94, v94, 2, v210
	v_med3_i32 v88, v88, 16, v239
	ds_read_b32 v94, v94
	v_lshlrev_b32_e32 v88, 2, v88
	v_add3_u32 v88, v210, v88, s12
	ds_read_b32 v88, v88
	v_cmp_lt_i32_e32 vcc, 34, v107
	s_waitcnt lgkmcnt(1)
	v_add_f32_e32 v94, v93, v94
	v_exp_f32_e32 v94, v94
	s_and_b64 vcc, s[0:1], vcc
	s_waitcnt lgkmcnt(0)
	v_add_f32_e32 v88, v69, v88
	v_exp_f32_e32 v95, v88
	v_cndmask_b32_e32 v88, 0, v94, vcc
	v_cmp_lt_i32_e32 vcc, 50, v107
	s_and_b64 vcc, s[0:1], vcc
	s_mov_b64 s[12:13], 0
	v_cndmask_b32_e32 v94, 0, v95, vcc
	v_add_f32_e32 v95, v88, v94
	v_add_f32_e32 v89, v89, v95
